# speedup vs baseline: 1.0508x; 1.0508x over previous
.LBB1_70:
	s_or_b64 exec, exec, s[4:5]
	v_cmp_gt_u32_e64 s[2:3], 32, v244
	v_mov_b32_e32 v59, 0
	v_mov_b32_e32 v6, 0
	s_waitcnt lgkmcnt(0)
	s_barrier
	s_and_saveexec_b64 s[4:5], s[2:3]
	v_mov_b32_e32 v0, 0x27610
	v_lshl_add_u32 v0, v244, 2, v0
	ds_read_b32 v6, v0
	s_or_b64 exec, exec, s[4:5]
	s_load_dwordx4 s[12:15], s[0:1], 0x8
	s_load_dwordx4 s[16:19], s[0:1], 0x58
	v_lshlrev_b32_e32 v60, 2, v244
	s_cmp_lg_u32 s7, 0
	v_add_u32_e32 v0, 0x27690, v60
	v_lshlrev_b32_e32 v58, 4, v174
	s_cselect_b64 s[28:29], -1, 0
	s_cmp_lg_u32 s6, 0
	v_accvgpr_write_b32 a143, v0
	s_waitcnt lgkmcnt(0)
	v_lshl_add_u64 v[0:1], s[12:13], 0, v[58:59]
	s_mov_b64 s[6:7], 0x60000
	v_lshl_add_u64 v[0:1], v[0:1], 0, s[6:7]
	v_lshl_add_u64 v[62:63], v[0:1], 0, v[120:121]
	s_mov_b64 s[6:7], 0x6000
	v_lshl_add_u64 v[2:3], v[62:63], 0, s[6:7]
	v_accvgpr_write_b32 a147, v3
	s_mov_b64 s[6:7], 0x6400
	v_accvgpr_write_b32 a146, v2
	v_lshl_add_u64 v[2:3], v[62:63], 0, s[6:7]
	v_accvgpr_write_b32 a149, v3
	s_mov_b64 s[6:7], 0x6800
	v_accvgpr_write_b32 a148, v2
	v_lshl_add_u64 v[2:3], v[62:63], 0, s[6:7]
	v_accvgpr_write_b32 a151, v3
	s_mov_b64 s[6:7], 0x6c00
	v_accvgpr_write_b32 a150, v2
	v_lshl_add_u64 v[2:3], v[62:63], 0, s[6:7]
	s_mov_b64 s[6:7], 0x1000
	v_accvgpr_write_b32 a153, v3
	v_lshl_add_u64 v[222:223], v[62:63], 0, s[6:7]
	s_mov_b64 s[6:7], 0x7000
	v_accvgpr_write_b32 a152, v2
	v_lshl_add_u64 v[2:3], v[62:63], 0, s[6:7]
	s_mov_b64 s[6:7], 0x1400
	v_accvgpr_write_b32 a155, v3
	v_lshl_add_u64 v[76:77], v[62:63], 0, s[6:7]
	s_mov_b64 s[6:7], 0x7400
	v_accvgpr_write_b32 a154, v2
	v_lshl_add_u64 v[2:3], v[62:63], 0, s[6:7]
	v_accvgpr_write_b32 a157, v3
	s_mov_b64 s[6:7], 0x18000
	v_accvgpr_write_b32 a156, v2
	v_lshl_add_u64 v[2:3], v[62:63], 0, s[6:7]
	v_accvgpr_write_b32 a159, v3
	s_mov_b64 s[6:7], 0x18400
	v_accvgpr_write_b32 a158, v2
	v_lshl_add_u64 v[2:3], v[62:63], 0, s[6:7]
	v_accvgpr_write_b32 a161, v3
	s_mov_b64 s[6:7], 0x18800
	v_accvgpr_write_b32 a160, v2
	v_lshl_add_u64 v[2:3], v[62:63], 0, s[6:7]
	v_accvgpr_write_b32 a163, v3
	s_mov_b64 s[6:7], 0x18c00
	v_accvgpr_write_b32 a162, v2
	v_lshl_add_u64 v[2:3], v[62:63], 0, s[6:7]
	v_accvgpr_write_b32 a165, v3
	s_mov_b64 s[6:7], 0x19000
	v_accvgpr_write_b32 a164, v2
	v_lshl_add_u64 v[2:3], v[62:63], 0, s[6:7]
	v_accvgpr_write_b32 a167, v3
	s_mov_b64 s[6:7], 0x19400
	v_accvgpr_write_b32 a166, v2
	v_lshl_add_u64 v[2:3], v[62:63], 0, s[6:7]
	v_accvgpr_write_b32 a169, v3
	v_lshl_add_u64 v[0:1], v[0:1], 0, v[122:123]
	s_mov_b64 s[6:7], 0x48000
	v_accvgpr_write_b32 a168, v2
	v_lshl_add_u64 v[2:3], v[0:1], 0, s[6:7]
	v_accvgpr_write_b32 a171, v3
	s_mov_b64 s[8:9], 0x48400
	v_accvgpr_write_b32 a170, v2
	v_lshl_add_u64 v[2:3], v[0:1], 0, s[8:9]
	v_accvgpr_write_b32 a173, v3
	s_mov_b64 s[8:9], 0x48800
	v_accvgpr_write_b32 a172, v2
	v_lshl_add_u64 v[2:3], v[0:1], 0, s[8:9]
	v_accvgpr_write_b32 a175, v3
	s_mov_b64 s[8:9], 0x48c00
	v_accvgpr_write_b32 a174, v2
	v_lshl_add_u64 v[2:3], v[0:1], 0, s[8:9]
	v_accvgpr_write_b32 a177, v3
	v_accvgpr_write_b32 a176, v2
	v_lshl_add_u64 v[2:3], v[222:223], 0, v[120:121]
	v_lshl_add_u64 v[4:5], v[2:3], 0, s[6:7]
	v_accvgpr_write_b32 a179, v5
	v_accvgpr_write_b32 a178, v4
	v_lshl_add_u64 v[4:5], v[76:77], 0, v[120:121]
	v_lshl_add_u64 v[8:9], v[4:5], 0, s[6:7]
	v_accvgpr_write_b32 a181, v9
	s_mov_b64 s[6:7], 0x49800
	v_accvgpr_write_b32 a180, v8
	v_lshl_add_u64 v[8:9], v[0:1], 0, s[6:7]
	v_accvgpr_write_b32 a183, v9
	s_mov_b64 s[6:7], 0x49c00
	v_accvgpr_write_b32 a182, v8
	v_lshl_add_u64 v[8:9], v[0:1], 0, s[6:7]
	v_accvgpr_write_b32 a185, v9
	s_mov_b64 s[6:7], 0x4a000
	v_accvgpr_write_b32 a184, v8
	v_lshl_add_u64 v[8:9], v[0:1], 0, s[6:7]
	v_accvgpr_write_b32 a187, v9
	s_mov_b64 s[6:7], 0x4a400
	v_accvgpr_write_b32 a186, v8
	v_lshl_add_u64 v[8:9], v[0:1], 0, s[6:7]
	v_accvgpr_write_b32 a189, v9
	s_mov_b64 s[6:7], 0x4a800
	v_accvgpr_write_b32 a188, v8
	v_lshl_add_u64 v[8:9], v[0:1], 0, s[6:7]
	v_accvgpr_write_b32 a191, v9
	s_mov_b64 s[6:7], 0x4ac00
	v_accvgpr_write_b32 a190, v8
	v_lshl_add_u64 v[8:9], v[0:1], 0, s[6:7]
	v_accvgpr_write_b32 a193, v9
	s_mov_b64 s[6:7], 0x30000
	v_accvgpr_write_b32 a192, v8
	v_lshl_add_u64 v[8:9], v[0:1], 0, s[6:7]
	v_accvgpr_write_b32 a195, v9
	s_mov_b64 s[8:9], 0x3c000
	v_accvgpr_write_b32 a194, v8
	v_lshl_add_u64 v[8:9], v[0:1], 0, s[8:9]
	v_accvgpr_write_b32 a197, v9
	s_mov_b64 s[8:9], 0x30400
	v_accvgpr_write_b32 a196, v8
	v_lshl_add_u64 v[8:9], v[0:1], 0, s[8:9]
	v_accvgpr_write_b32 a199, v9
	s_mov_b64 s[8:9], 0x3c400
	v_accvgpr_write_b32 a198, v8
	v_lshl_add_u64 v[8:9], v[0:1], 0, s[8:9]
	v_accvgpr_write_b32 a201, v9
	s_mov_b64 s[8:9], 0x30800
	v_accvgpr_write_b32 a200, v8
	v_lshl_add_u64 v[8:9], v[0:1], 0, s[8:9]
	v_accvgpr_write_b32 a203, v9
	s_mov_b64 s[8:9], 0x3c800
	v_accvgpr_write_b32 a202, v8
	v_lshl_add_u64 v[8:9], v[0:1], 0, s[8:9]
	v_accvgpr_write_b32 a205, v9
	s_mov_b64 s[8:9], 0x30c00
	v_accvgpr_write_b32 a204, v8
	v_lshl_add_u64 v[8:9], v[0:1], 0, s[8:9]
	v_accvgpr_write_b32 a207, v9
	s_mov_b64 s[8:9], 0x3cc00
	v_lshl_add_u64 v[2:3], v[2:3], 0, s[6:7]
	v_accvgpr_write_b32 a206, v8
	v_lshl_add_u64 v[8:9], v[0:1], 0, s[8:9]
	v_accvgpr_write_b32 a211, v3
	s_mov_b64 s[8:9], 0x3d000
	v_accvgpr_write_b32 a210, v2
	v_lshl_add_u64 v[2:3], v[0:1], 0, s[8:9]
	v_accvgpr_write_b32 a213, v3
	v_accvgpr_write_b32 a212, v2
	v_lshl_add_u64 v[2:3], v[4:5], 0, s[6:7]
	v_accvgpr_write_b32 a215, v3
	s_mov_b64 s[6:7], 0x3d400
	v_accvgpr_write_b32 a214, v2
	v_lshl_add_u64 v[2:3], v[0:1], 0, s[6:7]
	v_accvgpr_write_b32 a217, v3
	s_mov_b64 s[6:7], 0x31800
	v_accvgpr_write_b32 a216, v2
	v_lshl_add_u64 v[2:3], v[0:1], 0, s[6:7]
	v_accvgpr_write_b32 a219, v3
	s_mov_b64 s[6:7], 0x3d800
	v_accvgpr_write_b32 a218, v2
	v_lshl_add_u64 v[2:3], v[0:1], 0, s[6:7]
	v_accvgpr_write_b32 a221, v3
	s_mov_b64 s[6:7], 0x31c00
	v_accvgpr_write_b32 a220, v2
	v_lshl_add_u64 v[2:3], v[0:1], 0, s[6:7]
	v_accvgpr_write_b32 a223, v3
	s_mov_b64 s[6:7], 0x3dc00
	v_accvgpr_write_b32 a222, v2
	v_lshl_add_u64 v[2:3], v[0:1], 0, s[6:7]
	v_accvgpr_write_b32 a225, v3
	s_mov_b64 s[6:7], 0x32000
	v_accvgpr_write_b32 a224, v2
	v_lshl_add_u64 v[2:3], v[0:1], 0, s[6:7]
	v_accvgpr_write_b32 a227, v3
	s_mov_b64 s[6:7], 0x3e000
	v_accvgpr_write_b32 a226, v2
	v_lshl_add_u64 v[2:3], v[0:1], 0, s[6:7]
	v_accvgpr_write_b32 a229, v3
	s_mov_b64 s[6:7], 0x32400
	v_accvgpr_write_b32 a228, v2
	v_lshl_add_u64 v[2:3], v[0:1], 0, s[6:7]
	v_accvgpr_write_b32 a231, v3
	s_mov_b64 s[6:7], 0x3e400
	v_accvgpr_write_b32 a230, v2
	v_lshl_add_u64 v[2:3], v[0:1], 0, s[6:7]
	v_accvgpr_write_b32 a233, v3
	s_mov_b64 s[6:7], 0x32800
	v_accvgpr_write_b32 a232, v2
	v_lshl_add_u64 v[2:3], v[0:1], 0, s[6:7]
	v_accvgpr_write_b32 a235, v3
	s_mov_b64 s[6:7], 0x3e800
	v_accvgpr_write_b32 a234, v2
	v_lshl_add_u64 v[2:3], v[0:1], 0, s[6:7]
	s_mov_b64 s[6:7], 0x32c00
	s_mul_hi_u32 s4, s26, 0x13b13b14
	v_lshl_add_u64 v[4:5], v[0:1], 0, s[6:7]
	s_mov_b64 s[6:7], 0x3ec00
	s_mul_i32 s4, s4, 13
	v_lshl_add_u64 v[166:167], v[0:1], 0, s[6:7]
	s_load_dwordx2 s[6:7], s[0:1], 0x70
	s_cselect_b64 s[30:31], -1, 0
	s_sub_i32 s4, s26, s4
	v_lshlrev_b32_e32 v0, 7, v170
	s_add_i32 s5, s4, 1
	s_add_i32 s12, s4, 2
	s_add_i32 s34, s4, 3
	s_add_i32 s37, s4, 4
	s_add_i32 s40, s4, 5
	s_add_i32 s43, s4, 6
	s_add_i32 s46, s4, 7
	s_add_i32 s49, s4, 8
	s_add_i32 s52, s4, 9
	s_add_i32 s55, s4, 10
	s_add_i32 s58, s4, 11
	s_add_i32 s61, s4, 12
	v_lshl_or_b32 v58, s33, 9, v0
	s_lshl_b32 s10, s5, 10
	s_lshl_b32 s13, s12, 10
	s_lshl_b32 s35, s34, 10
	s_lshl_b32 s38, s37, 10
	s_lshl_b32 s41, s40, 10
	s_lshl_b32 s44, s43, 10
	s_lshl_b32 s47, s46, 10
	s_lshl_b32 s50, s49, 10
	s_lshl_b32 s53, s52, 10
	s_lshl_b32 s56, s55, 10
	s_lshl_b32 s59, s58, 10
	s_lshl_b32 s8, s61, 10
	s_mov_b32 s27, 0
	s_lshl_b32 s24, s26, 4
	v_accvgpr_write_b32 a145, v0
	v_lshl_add_u64 v[0:1], s[18:19], 0, v[58:59]
	s_lshl_b32 s18, s4, 10
	s_add_i32 s11, s10, 0xffffcc00
	s_add_i32 s19, s13, 0xffffcc00
	s_add_i32 s36, s35, 0xffffcc00
	s_add_i32 s39, s38, 0xffffcc00
	s_add_i32 s42, s41, 0xffffcc00
	s_add_i32 s45, s44, 0xffffcc00
	s_add_i32 s48, s47, 0xffffcc00
	s_add_i32 s51, s50, 0xffffcc00
	s_add_i32 s54, s53, 0xffffcc00
	s_add_i32 s57, s56, 0xffffcc00
	s_add_i32 s60, s59, 0xffffcc00
	s_add_i32 s62, s8, 0xffffcc00
	s_mul_i32 s8, s33, 0x640
	s_mov_b32 s25, s27
	s_waitcnt lgkmcnt(0)
	s_add_u32 s8, s6, s8
	s_addc_u32 s9, s7, 0
	s_lshl_b64 s[6:7], s[24:25], 2
	s_add_u32 s8, s8, s6
	s_addc_u32 s9, s9, s7
	s_lshl_b32 s5, s5, 6
	s_add_i32 s6, s5, 0xfffffcc0
	s_cmp_gt_u32 s4, 11
	s_cselect_b32 s25, s11, s10
	s_cselect_b32 s10, s6, s5
	s_lshl_b32 s5, s12, 6
	s_add_i32 s6, s5, 0xfffffcc0
	s_cmp_gt_u32 s4, 10
	s_cselect_b32 s19, s19, s13
	s_cselect_b32 s11, s6, s5
	s_lshl_b32 s5, s34, 6
	s_add_i32 s6, s5, 0xfffffcc0
	s_cmp_gt_u32 s4, 9
	s_cselect_b32 s34, s36, s35
	s_cselect_b32 s12, s6, s5
	s_lshl_b32 s5, s37, 6
	s_add_i32 s6, s5, 0xfffffcc0
	s_cmp_gt_u32 s4, 8
	s_cselect_b32 s35, s39, s38
	s_cselect_b32 s13, s6, s5
	s_lshl_b32 s5, s40, 6
	s_add_i32 s6, s5, 0xfffffcc0
	s_cmp_gt_u32 s4, 7
	s_cselect_b32 s36, s42, s41
	s_cselect_b32 s37, s6, s5
	s_lshl_b32 s5, s43, 6
	s_add_i32 s6, s5, 0xfffffcc0
	s_cmp_gt_u32 s4, 6
	s_cselect_b32 s38, s45, s44
	s_cselect_b32 s39, s6, s5
	s_lshl_b32 s5, s46, 6
	s_add_i32 s6, s5, 0xfffffcc0
	s_cmp_gt_u32 s4, 5
	s_cselect_b32 s40, s48, s47
	s_cselect_b32 s41, s6, s5
	s_lshl_b32 s5, s49, 6
	s_add_i32 s6, s5, 0xfffffcc0
	s_cmp_gt_u32 s4, 4
	s_cselect_b32 s42, s51, s50
	s_cselect_b32 s43, s6, s5
	s_lshl_b32 s5, s52, 6
	s_add_i32 s6, s5, 0xfffffcc0
	s_cmp_gt_u32 s4, 3
	s_cselect_b32 s44, s54, s53
	s_cselect_b32 s45, s6, s5
	s_lshl_b32 s5, s55, 6
	s_add_i32 s6, s5, 0xfffffcc0
	s_cmp_gt_u32 s4, 2
	s_cselect_b32 s46, s57, s56
	s_cselect_b32 s47, s6, s5
	s_lshl_b32 s5, s58, 6
	s_add_i32 s6, s5, 0xfffffcc0
	s_cmp_gt_u32 s4, 1
	v_accvgpr_write_b32 a209, v9
	v_accvgpr_write_b32 a237, v3
	s_cselect_b32 s48, s60, s59
	s_cselect_b32 s49, s6, s5
	s_lshl_b32 s5, s61, 6
	v_accvgpr_write_b32 a208, v8
	v_accvgpr_write_b32 a236, v2
	v_min_u32_e32 v2, 24, v174
	v_lshl_or_b32 v8, s33, 2, v170
	s_add_i32 s50, s5, 0xfffffcc0
	v_lshlrev_b32_e32 v58, 2, v2
	v_mul_u32_u24_e32 v2, 0x3400, v8
	s_cmp_eq_u32 s4, 0
	v_or_b32_e32 v2, v2, v180
	s_cselect_b32 s51, 0x3000, s62
	v_mov_b32_e32 v61, v59
	s_waitcnt vmcnt(0)
	v_accvgpr_read_b32 v3, a142
	v_lshlrev_b32_e32 v7, 2, v183
	v_add_u32_e32 v194, s18, v2
	v_add_u32_e32 v195, s25, v2
	v_add_u32_e32 v196, s19, v2
	v_add_u32_e32 v197, s34, v2
	v_add_u32_e32 v198, s35, v2
	v_add_u32_e32 v199, s36, v2
	v_add_u32_e32 v200, s38, v2
	v_add_u32_e32 v201, s40, v2
	v_add_u32_e32 v202, s42, v2
	v_add_u32_e32 v203, s44, v2
	v_add_u32_e32 v204, s46, v2
	v_add_u32_e32 v205, s48, v2
	v_add_u32_e32 v206, s51, v2
	v_lshl_add_u64 v[170:171], s[8:9], 0, v[60:61]
	v_lshl_or_b32 v213, s37, 4, v180
	s_cselect_b32 s8, 0x300, s50
	v_and_b32_e32 v2, 16, v244
	v_mul_f32_e32 v3, v3, v6
	v_or_b32_e32 v6, s24, v181
	v_or_b32_e32 v11, 32, v8
	s_bfe_u32 s37, s26, 0x1b0001
	v_lshl_add_u64 v[168:169], v[0:1], 0, v[58:59]
	v_lshl_or_b32 v2, v2, 2, v7
	v_mad_u32_u24 v58, v11, 13, s37
	v_lshlrev_b32_e32 v6, 1, v6
	v_accvgpr_write_b32 a238, v3
	v_accvgpr_write_b32 a239, v2
	v_lshlrev_b64 v[2:3], 10, v[58:59]
	v_and_or_b32 v6, v6, 48, v183
	v_lshl_add_u64 v[2:3], s[16:17], 0, v[2:3]
	v_lshlrev_b32_e32 v58, 4, v6
	v_and_b32_e32 v6, 4, v111
	v_accvgpr_write_b32 a144, v7
	v_lshl_add_u64 v[2:3], v[2:3], 0, v[58:59]
	v_lshlrev_b32_e32 v6, 1, v6
	v_mov_b32_e32 v7, v59
	s_lshl_b32 s26, s26, 2
	v_lshl_or_b32 v209, s10, 4, v180
	v_lshl_or_b32 v210, s11, 4, v180
	v_lshl_or_b32 v211, s12, 4, v180
	v_lshl_or_b32 v212, s13, 4, v180
	v_cmp_gt_u32_e64 s[10:11], 16, v174
	v_lshl_add_u64 v[172:173], v[2:3], 0, v[6:7]
	v_lshlrev_b32_e32 v2, 1, v175
	v_cmp_eq_u32_e64 s[12:13], 0, v174
	v_lshl_add_u64 v[174:175], v[0:1], 0, s[26:27]
	v_mul_u32_u24_e32 v0, 0x3400, v11
	v_or_b32_e32 v0, v0, v180
	v_add_u32_e32 v229, s18, v0
	v_add_u32_e32 v230, s25, v0
	v_add_u32_e32 v231, s19, v0
	v_add_u32_e32 v232, s34, v0
	v_add_u32_e32 v233, s35, v0
	v_add_u32_e32 v234, s36, v0
	v_add_u32_e32 v235, s38, v0
	v_add_u32_e32 v236, s40, v0
	v_add_u32_e32 v237, s42, v0
	v_add_u32_e32 v238, s44, v0
	v_add_u32_e32 v239, s46, v0
	v_add_u32_e32 v240, s48, v0
	v_add_u32_e32 v241, s51, v0
	v_add_u32_e32 v1, 0x3000, v0
	v_add_u32_e32 v9, 0xfff98000, v1
	v_and_b32_e32 v10, 0x200, v180
	v_cmp_eq_u32_e32 vcc, v9, v194
	s_nop 1
	v_cndmask_b32_e32 v12, 0, v10, vcc
	v_sub_u32_e32 v194, v194, v12
	v_cmp_eq_u32_e32 vcc, v9, v195
	s_nop 1
	v_cndmask_b32_e32 v12, 0, v10, vcc
	v_sub_u32_e32 v195, v195, v12
	v_cmp_eq_u32_e32 vcc, v9, v196
	s_nop 1
	v_cndmask_b32_e32 v12, 0, v10, vcc
	v_sub_u32_e32 v196, v196, v12
	v_cmp_eq_u32_e32 vcc, v9, v197
	s_nop 1
	v_cndmask_b32_e32 v12, 0, v10, vcc
	v_sub_u32_e32 v197, v197, v12
	v_cmp_eq_u32_e32 vcc, v9, v198
	s_nop 1
	v_cndmask_b32_e32 v12, 0, v10, vcc
	v_sub_u32_e32 v198, v198, v12
	v_cmp_eq_u32_e32 vcc, v9, v199
	s_nop 1
	v_cndmask_b32_e32 v12, 0, v10, vcc
	v_sub_u32_e32 v199, v199, v12
	v_cmp_eq_u32_e32 vcc, v9, v200
	s_nop 1
	v_cndmask_b32_e32 v12, 0, v10, vcc
	v_sub_u32_e32 v200, v200, v12
	v_cmp_eq_u32_e32 vcc, v9, v201
	s_nop 1
	v_cndmask_b32_e32 v12, 0, v10, vcc
	v_sub_u32_e32 v201, v201, v12
	v_cmp_eq_u32_e32 vcc, v9, v202
	s_nop 1
	v_cndmask_b32_e32 v12, 0, v10, vcc
	v_sub_u32_e32 v202, v202, v12
	v_cmp_eq_u32_e32 vcc, v9, v203
	s_nop 1
	v_cndmask_b32_e32 v12, 0, v10, vcc
	v_sub_u32_e32 v203, v203, v12
	v_cmp_eq_u32_e32 vcc, v9, v204
	s_nop 1
	v_cndmask_b32_e32 v12, 0, v10, vcc
	v_sub_u32_e32 v204, v204, v12
	v_cmp_eq_u32_e32 vcc, v9, v205
	s_nop 1
	v_cndmask_b32_e32 v12, 0, v10, vcc
	v_sub_u32_e32 v205, v205, v12
	v_cmp_eq_u32_e32 vcc, v9, v206
	s_nop 1
	v_cndmask_b32_e32 v12, 0, v10, vcc
	v_sub_u32_e32 v206, v206, v12
	v_cmp_eq_u32_e32 vcc, v1, v229
	s_nop 1
	v_cndmask_b32_e32 v12, 0, v10, vcc
	v_sub_u32_e32 v229, v229, v12
	v_cmp_eq_u32_e32 vcc, v1, v230
	s_nop 1
	v_cndmask_b32_e32 v12, 0, v10, vcc
	v_sub_u32_e32 v230, v230, v12
	v_cmp_eq_u32_e32 vcc, v1, v231
	s_nop 1
	v_cndmask_b32_e32 v12, 0, v10, vcc
	v_sub_u32_e32 v231, v231, v12
	v_cmp_eq_u32_e32 vcc, v1, v232
	s_nop 1
	v_cndmask_b32_e32 v12, 0, v10, vcc
	v_sub_u32_e32 v232, v232, v12
	v_cmp_eq_u32_e32 vcc, v1, v233
	s_nop 1
	v_cndmask_b32_e32 v12, 0, v10, vcc
	v_sub_u32_e32 v233, v233, v12
	v_cmp_eq_u32_e32 vcc, v1, v234
	s_nop 1
	v_cndmask_b32_e32 v12, 0, v10, vcc
	v_sub_u32_e32 v234, v234, v12
	v_cmp_eq_u32_e32 vcc, v1, v235
	s_nop 1
	v_cndmask_b32_e32 v12, 0, v10, vcc
	v_sub_u32_e32 v235, v235, v12
	v_cmp_eq_u32_e32 vcc, v1, v236
	s_nop 1
	v_cndmask_b32_e32 v12, 0, v10, vcc
	v_sub_u32_e32 v236, v236, v12
	v_cmp_eq_u32_e32 vcc, v1, v237
	s_nop 1
	v_cndmask_b32_e32 v12, 0, v10, vcc
	v_sub_u32_e32 v237, v237, v12
	v_cmp_eq_u32_e32 vcc, v1, v238
	s_nop 1
	v_cndmask_b32_e32 v12, 0, v10, vcc
	v_sub_u32_e32 v238, v238, v12
	v_cmp_eq_u32_e32 vcc, v1, v239
	s_nop 1
	v_cndmask_b32_e32 v12, 0, v10, vcc
	v_sub_u32_e32 v239, v239, v12
	v_cmp_eq_u32_e32 vcc, v1, v240
	s_nop 1
	v_cndmask_b32_e32 v12, 0, v10, vcc
	v_sub_u32_e32 v240, v240, v12
	v_cmp_eq_u32_e32 vcc, v1, v241
	s_nop 1
	v_cndmask_b32_e32 v12, 0, v10, vcc
	v_sub_u32_e32 v241, v241, v12
	v_mad_u32_u24 v0, v8, 13, s37
	v_mov_b32_e32 v1, v59
	v_lshlrev_b64 v[0:1], 10, v[0:1]
	v_lshl_add_u64 v[0:1], s[16:17], 0, v[0:1]
	v_mov_b32_e32 v111, v59
	v_lshl_add_u64 v[0:1], v[0:1], 0, v[58:59]
	v_mul_u32_u24_e32 v61, 0x320, v183
	v_lshlrev_b32_e32 v9, 1, v113
	v_lshlrev_b32_e32 v10, 1, v181
	v_lshlrev_b32_e32 v225, 2, v181
	v_lshl_add_u64 v[176:177], s[14:15], 0, v[110:111]
	v_mul_u32_u24_e32 v111, 0x220, v183
	v_lshl_add_u64 v[178:179], v[0:1], 0, v[6:7]
	v_mul_u32_u24_e32 v0, 0x320, v181
	s_movk_i32 s52, 0x320
	v_add3_u32 v221, v61, v9, v10
	v_lshlrev_b32_e32 v224, 8, v181
	v_sub_u32_e32 v3, v110, v2
	v_mul_u32_u24_e32 v12, 0x220, v181
	v_add3_u32 v9, v111, v9, v10
	s_mov_b32 s14, 0xf010
	v_lshl_add_u32 v1, v113, 2, v225
	v_add_u32_e32 v245, v2, v0
	v_mbcnt_lo_u32_b32 v0, -1, 0
	v_add_u32_e32 v189, 0x27010, v60
	v_cmp_lt_u32_e64 s[4:5], 15, v244
	v_cmp_gt_u32_e64 s[6:7], 16, v244
	v_and_b32_e32 v207, 48, v244
	v_or_b32_e32 v208, s18, v180
	v_lshl_or_b32 v214, s39, 4, v180
	v_lshl_or_b32 v215, s41, 4, v180
	v_lshl_or_b32 v216, s43, 4, v180
	v_lshl_or_b32 v217, s45, 4, v180
	v_lshl_or_b32 v218, s47, 4, v180
	v_lshl_or_b32 v219, s49, 4, v180
	v_lshl_or_b32 v220, s8, 4, v180
	v_cmp_gt_u32_e64 s[8:9], 48, v244
	v_or_b32_e32 v226, 0x100, v224
	v_or_b32_e32 v227, 0x200, v224
	v_or_b32_e32 v228, 0x300, v224
	v_or_b32_e32 v242, v224, v110
	v_add3_u32 v58, v180, v182, s14
	v_mad_u32_u24 v243, v181, s52, v2
	v_accvgpr_write_b32 a136, v183
	v_cmp_eq_u32_e64 s[14:15], 0, v183
	v_accvgpr_write_b32 a240, v1
	v_mov_b32_e32 v113, v112
	v_mbcnt_hi_u32_b32 v246, -1, v0
	v_add_u32_e32 v247, v3, v12
	v_add_u32_e32 v248, 0x3000, v9
	s_mov_b32 s25, 0
	s_mov_b32 s64, 0x40004000
	s_mov_b32 s65, 0
	s_mov_b32 s40, 0
	s_branch .LBB1_75

.LBB1_77:
	s_add_i32 s71, s40, 0
	global_load_dword v6, v[168:169], off sc1
	v_add_u32_e32 v249, v61, v207
	ds_read_b128 v[64:67], v249
	ds_read_b128 v[68:71], v249 offset:64
	ds_read_b128 v[78:81], v249 offset:256
	ds_read_b128 v[82:85], v249 offset:320
	ds_read_b128 v[86:89], v249 offset:512
	ds_read_b128 v[90:93], v249 offset:576
	s_waitcnt lgkmcnt(5)
	v_mfma_f32_16x16x32_f16 a[0:3], v[64:67], a[8:11], 0
	s_waitcnt lgkmcnt(4)
	v_mfma_f32_16x16x32_f16 a[0:3], v[68:71], a[12:15], a[0:3]
	s_waitcnt lgkmcnt(3)
	v_mfma_f32_16x16x32_f16 a[0:3], v[78:81], a[24:27], a[0:3]
	s_waitcnt lgkmcnt(2)
	v_mfma_f32_16x16x32_f16 a[0:3], v[82:85], a[28:31], a[0:3]
	s_waitcnt lgkmcnt(1)
	v_mfma_f32_16x16x32_f16 a[0:3], v[86:89], a[40:43], a[0:3]
	s_waitcnt lgkmcnt(0)
	v_mfma_f32_16x16x32_f16 a[4:7], v[90:93], a[44:47], a[0:3]
	v_mfma_f32_16x16x32_f16 a[0:3], v[64:67], a[16:19], 0
	v_mfma_f32_16x16x32_f16 a[0:3], v[68:71], a[20:23], a[0:3]
	v_mfma_f32_16x16x32_f16 a[0:3], v[78:81], a[32:35], a[0:3]
	v_mfma_f32_16x16x32_f16 a[0:3], v[82:85], a[36:39], a[0:3]
	v_mfma_f32_16x16x32_f16 a[0:3], v[86:89], a[48:51], a[0:3]
	v_mfma_f32_16x16x32_f16 a[0:3], v[90:93], a[52:55], a[0:3]
	global_load_dword v7, v[168:169], off sc1
.Lpl0_loop:
	s_waitcnt vmcnt(1)
	v_cmp_le_u32_e64 s[66:67], s71, v6
	s_cmp_eq_u64 s[66:67], exec
	s_cbranch_scc1 .Lpl0_done
	s_waitcnt vmcnt(0)
	v_cmp_le_u32_e64 s[66:67], s71, v7
	s_cmp_eq_u64 s[66:67], exec
	s_cbranch_scc1 .Lpl0_done
	s_add_i32 s65, s65, 1
	s_cmp_gt_u32 s65, 0xffff
	s_cbranch_scc1 .Lpl0_done
	global_load_dword v6, v[168:169], off sc1
	s_sleep 2
	global_load_dword v7, v[168:169], off sc1
	s_branch .Lpl0_loop
.Lpl0_done:
.LBB1_87:
	s_cmp_gt_u32 s25, 11
	s_cselect_b64 s[18:19], -1, 0
	s_cmp_lt_u32 s25, 12
	s_cselect_b64 s[36:37], -1, 0
	s_and_b64 s[16:17], s[18:19], exec
	s_cselect_b32 s42, 4, 0
	buffer_load_dwordx4 v[54:57], v194, s[20:23], 0 offen sc1
	buffer_load_dwordx4 v[50:53], v195, s[20:23], 0 offen sc1
	buffer_load_dwordx4 v[46:49], v196, s[20:23], 0 offen sc1
	buffer_load_dwordx4 v[42:45], v197, s[20:23], 0 offen sc1
	buffer_load_dwordx4 v[38:41], v198, s[20:23], 0 offen sc1
	buffer_load_dwordx4 v[34:37], v199, s[20:23], 0 offen sc1
	buffer_load_dwordx4 v[30:33], v200, s[20:23], 0 offen sc1
	buffer_load_dwordx4 v[26:29], v201, s[20:23], 0 offen sc1
	buffer_load_dwordx4 v[22:25], v202, s[20:23], 0 offen sc1
	buffer_load_dwordx4 v[18:21], v203, s[20:23], 0 offen sc1
	buffer_load_dwordx4 v[14:17], v204, s[20:23], 0 offen sc1
	buffer_load_dwordx4 v[10:13], v205, s[20:23], 0 offen sc1
	buffer_load_dwordx4 v[6:9], v206, s[20:23], 0 offen sc1
	s_lshl_b32 s26, s42, 3
	s_load_dwordx2 s[16:17], s[0:1], s26 offset:0x18
	s_add_u32 s34, s0, s26
	s_addc_u32 s35, s1, 0
	s_and_b64 s[38:39], s[18:19], exec
	s_cselect_b32 s26, 0x1800, 0
	v_lshl_add_u64 v[250:251], v[176:177], 0, s[26:27]
	s_waitcnt lgkmcnt(0)
	global_load_dword v180, v110, s[16:17]
	global_load_dword v252, v110, s[16:17] offset:256
	global_load_dword v182, v[250:251], off
	global_load_dword v183, v[250:251], off offset:512
	global_load_dword v186, v[250:251], off offset:1024
	global_load_dword v253, v[250:251], off offset:1280
	global_load_dword v255, v[250:251], off offset:768
	global_load_dword v254, v[250:251], off offset:256
	s_nor_b64 s[38:39], s[18:19], s[4:5]
	v_mov_b32_e32 v185, 0
	v_mov_b32_e32 v184, 0
	v_mov_b32_e32 v181, 0
	s_and_saveexec_b64 s[16:17], s[38:39]
	s_cbranch_execz .LBB1_89
	s_mul_i32 s26, s25, 0x3200
	v_lshl_add_u64 v[250:251], v[170:171], 0, s[26:27]
	global_load_dword v181, v[250:251], off
	v_lshl_add_u32 v250, s25, 7, v189
	ds_read2_b32 v[184:185], v250 offset1:16
.LBB1_89:
	s_or_b64 exec, exec, s[16:17]
	s_add_i32 s41, s25, -12
	s_and_b64 s[16:17], s[18:19], exec
	s_cselect_b32 s26, s41, s25
	s_cmp_lg_u32 s26, 0
	s_cselect_b64 s[16:17], -1, 0
	s_cmp_eq_u32 s26, 0
	s_cselect_b64 s[38:39], -1, 0
	ds_read_b128 v[64:67], v208 offset:34832
	ds_read_b128 v[68:71], v208 offset:48144
	ds_read_b128 v[78:81], v209 offset:34832
	ds_read_b128 v[82:85], v209 offset:48144
	ds_read_b128 v[86:89], v210 offset:34832
	ds_read_b128 v[90:93], v210 offset:48144
	ds_read_b128 v[94:97], v211 offset:34832
	ds_read_b128 v[98:101], v211 offset:48144
	ds_read_b128 v[190:193], v212 offset:34832
	ds_read_b128 v[102:105], v212 offset:48144
	ds_read_b128 v[106:109], v213 offset:34832
	ds_read_b128 v[114:117], v213 offset:48144
	ds_read_b128 v[118:121], v214 offset:34832
	ds_read_b128 v[122:125], v214 offset:48144
	ds_read_b128 v[126:129], v215 offset:34832
	ds_read_b128 v[130:133], v215 offset:48144
	ds_read_b128 v[134:137], v216 offset:34832
	ds_read_b128 v[138:141], v216 offset:48144
	ds_read_b128 v[142:145], v217 offset:34832
	ds_read_b128 v[146:149], v217 offset:48144
	ds_read_b128 v[150:153], v218 offset:34832
	ds_read_b128 v[154:157], v218 offset:48144
	ds_read_b128 v[158:161], v219 offset:34832
	ds_read_b128 v[162:165], v219 offset:48144
	ds_read_b128 v[72:75], v220 offset:34832
	ds_read_b128 v[0:3], v220 offset:48144
	s_andn2_b64 vcc, exec, s[36:37]
	s_mov_b64 s[36:37], -1
.Ltg0_entry:
	v_mov_b32_e32 v250, 0
	s_waitcnt vmcnt(20) lgkmcnt(14)
	v_or3_b32 v250, v250, v55, v57
	v_mfma_f32_16x16x32_f16 a[128:131], v[54:57], v[64:67], 0
	s_waitcnt vmcnt(19)
	v_or3_b32 v250, v250, v51, v53
	v_mfma_f32_16x16x32_f16 a[128:131], v[50:53], v[78:81], a[128:131]
	v_mfma_f32_16x16x32_f16 a[132:135], v[54:57], v[68:71], 0
	s_waitcnt vmcnt(18)
	v_or3_b32 v250, v250, v47, v49
	v_mfma_f32_16x16x32_f16 a[128:131], v[46:49], v[86:89], a[128:131]
	v_mfma_f32_16x16x32_f16 a[132:135], v[50:53], v[82:85], a[132:135]
	s_waitcnt vmcnt(17)
	v_or3_b32 v250, v250, v43, v45
	v_mfma_f32_16x16x32_f16 a[128:131], v[42:45], v[94:97], a[128:131]
	v_mfma_f32_16x16x32_f16 a[132:135], v[46:49], v[90:93], a[132:135]
	s_waitcnt vmcnt(16)
	v_or3_b32 v250, v250, v39, v41
	v_mfma_f32_16x16x32_f16 a[128:131], v[38:41], v[190:193], a[128:131]
	v_mfma_f32_16x16x32_f16 a[132:135], v[42:45], v[98:101], a[132:135]
	s_waitcnt vmcnt(15)
	v_or3_b32 v250, v250, v35, v37
	v_mfma_f32_16x16x32_f16 a[128:131], v[34:37], v[106:109], a[128:131]
	v_mfma_f32_16x16x32_f16 a[132:135], v[38:41], v[102:105], a[132:135]
	s_waitcnt vmcnt(14) lgkmcnt(13)
	v_or3_b32 v250, v250, v31, v33
	v_mfma_f32_16x16x32_f16 a[128:131], v[30:33], v[118:121], a[128:131]
	v_mfma_f32_16x16x32_f16 a[132:135], v[34:37], v[114:117], a[132:135]
	s_waitcnt vmcnt(13) lgkmcnt(11)
	v_or3_b32 v250, v250, v27, v29
	v_mfma_f32_16x16x32_f16 a[128:131], v[26:29], v[126:129], a[128:131]
	v_mfma_f32_16x16x32_f16 a[132:135], v[30:33], v[122:125], a[132:135]
	s_waitcnt vmcnt(12) lgkmcnt(9)
	v_or3_b32 v250, v250, v23, v25
	v_mfma_f32_16x16x32_f16 a[128:131], v[22:25], v[134:137], a[128:131]
	v_mfma_f32_16x16x32_f16 a[132:135], v[26:29], v[130:133], a[132:135]
	s_waitcnt vmcnt(11) lgkmcnt(7)
	v_or3_b32 v250, v250, v19, v21
	v_mfma_f32_16x16x32_f16 a[128:131], v[18:21], v[142:145], a[128:131]
	v_mfma_f32_16x16x32_f16 a[132:135], v[22:25], v[138:141], a[132:135]
	s_waitcnt vmcnt(10) lgkmcnt(5)
	v_or3_b32 v250, v250, v15, v17
	v_mfma_f32_16x16x32_f16 a[128:131], v[14:17], v[150:153], a[128:131]
	v_mfma_f32_16x16x32_f16 a[132:135], v[18:21], v[146:149], a[132:135]
	s_waitcnt vmcnt(9) lgkmcnt(3)
	v_or3_b32 v250, v250, v11, v13
	v_mfma_f32_16x16x32_f16 a[128:131], v[10:13], v[158:161], a[128:131]
	v_mfma_f32_16x16x32_f16 a[132:135], v[14:17], v[154:157], a[132:135]
	s_waitcnt vmcnt(8) lgkmcnt(1)
	v_or3_b32 v250, v250, v7, v9
	v_mfma_f32_16x16x32_f16 a[128:131], v[6:9], v[72:75], a[128:131]
	v_mfma_f32_16x16x32_f16 a[132:135], v[10:13], v[162:165], a[132:135]
	v_and_b32_e32 v250, s64, v250
	v_cmp_ne_u32_e64 s[66:67], 0, v250
	s_cmp_lg_u64 s[66:67], 0
	s_cbranch_scc1 .Ltg0_redo
.Ltg0_go:
	s_nop 2
	v_accvgpr_read_b32 v10, a128
	v_accvgpr_read_b32 v11, a129
	v_accvgpr_read_b32 v12, a130
	v_accvgpr_read_b32 v13, a131
	s_waitcnt lgkmcnt(0)
	v_mfma_f32_16x16x32_f16 a[128:131], v[6:9], v[0:3], a[132:135]
	v_cvt_pk_f16_f32 v1, v12, v13
	v_cvt_pk_f16_f32 v0, v10, v11
	s_nop 5
	v_accvgpr_read_b32 v6, a128
	v_accvgpr_read_b32 v7, a129
	v_accvgpr_read_b32 v8, a130
	v_accvgpr_read_b32 v9, a131
	v_cvt_pk_f16_f32 v3, v8, v9
	v_cvt_pk_f16_f32 v2, v6, v7
	ds_write2_b64 v221, v[0:1], v[2:3] offset0:48 offset1:80
	s_cbranch_vccnz .LBB1_93
	s_and_saveexec_b64 s[36:37], s[6:7]
	s_cbranch_execz .LBB1_92
	v_add_u32_e32 v0, 0x8400, v60
	s_waitcnt vmcnt(0)
	ds_write2_b32 v0, v181, v184 offset1:16
	ds_write_b32 v60, v185 offset:33920

.LBB1_106:
	v_add_u32_e32 v184, v110, v224
	ds_read_b128 v[6:9], v225 offset:33792
	ds_read_b128 v[10:13], v225 offset:33856
	v_add_u32_e32 v250, v110, v226
	v_add_u32_e32 v185, v110, v227
	ds_read_b32 v20, v184 offset:21504
	ds_read_b32 v21, v250 offset:21504
	ds_read_b32 v22, v185 offset:21504
	ds_read_b128 v[14:17], v225 offset:33920
	v_add_u32_e32 v251, v110, v228
	ds_read_b32 v23, v251 offset:21504
	s_waitcnt lgkmcnt(6)
	v_mov_b32_e32 v0, v6
	s_waitcnt lgkmcnt(5)
	v_mov_b32_e32 v1, v10
	s_waitcnt vmcnt(5)
	v_mul_f32_e32 v2, v182, v6
	s_waitcnt vmcnt(4)
	v_pk_fma_f32 v[0:1], v[182:183], v[0:1], v[2:3] op_sel_hi:[1,1,0]
	s_waitcnt vmcnt(0) lgkmcnt(1)
	v_mul_f32_e32 v181, v186, v14
	v_accvgpr_read_b32 v0, a4
	v_pk_add_f32 v[0:1], v[180:181], v[0:1]
	v_mul_f32_e32 v2, v182, v7
	v_add_f32_e32 v0, v0, v1
	v_mul_f32_e32 v0, 0xbfb8aa3b, v0
	v_exp_f32_e32 v3, v0
	v_mov_b32_e32 v0, v7
	v_mov_b32_e32 v1, v11
	v_mul_f32_e32 v181, v186, v15
	v_pk_fma_f32 v[0:1], v[182:183], v[0:1], v[2:3] op_sel_hi:[1,1,0]
	v_mul_f32_e32 v2, v182, v8
	v_accvgpr_read_b32 v0, a5
	v_pk_add_f32 v[0:1], v[180:181], v[0:1]
	v_mul_f32_e32 v181, v186, v16
	v_add_f32_e32 v0, v0, v1
	v_mul_f32_e32 v0, 0xbfb8aa3b, v0
	v_exp_f32_e32 v0, v0
	v_add_f32_e32 v1, 1.0, v3
	v_rcp_f32_e32 v24, v1
	v_mov_b32_e32 v1, v12
	v_add_f32_e32 v3, 1.0, v0
	v_mov_b32_e32 v0, v8
	v_pk_fma_f32 v[0:1], v[182:183], v[0:1], v[2:3] op_sel_hi:[1,1,0]
	v_mul_f32_e32 v2, v182, v9
	v_accvgpr_read_b32 v0, a6
	v_pk_add_f32 v[0:1], v[180:181], v[0:1]
	v_mul_f32_e32 v181, v186, v17
	v_add_f32_e32 v0, v0, v1
	v_mul_f32_e32 v0, 0xbfb8aa3b, v0
	v_exp_f32_e32 v18, v0
	v_mov_b32_e32 v0, v9
	v_mov_b32_e32 v1, v13
	v_pk_fma_f32 v[0:1], v[182:183], v[0:1], v[2:3] op_sel_hi:[1,1,0]
	v_rcp_f32_e32 v25, v3
	v_accvgpr_read_b32 v0, a7
	v_pk_add_f32 v[0:1], v[180:181], v[0:1]
	s_andn2_b64 vcc, exec, s[28:29]
	v_add_f32_e32 v0, v0, v1
	v_mul_f32_e32 v0, 0xbfb8aa3b, v0
	v_exp_f32_e32 v0, v0
	v_add_f32_e32 v1, 1.0, v18
	v_rcp_f32_e32 v26, v1
	v_mul_f32_e32 v1, v21, v25
	v_add_f32_e32 v0, 1.0, v0
	v_rcp_f32_e32 v27, v0
	v_mul_f32_e32 v2, v22, v26
	v_mul_f32_e32 v0, v20, v24
	v_cvt_pk_f16_f32 v18, v0, v1
	s_waitcnt lgkmcnt(0)
	v_mul_f32_e32 v3, v23, v27
	v_cvt_pk_f16_f32 v19, v2, v3
	v_or_b32_e32 v19, s64, v19
	v_cndmask_b32_e64 v2, 0, 1, s[28:29]
	v_cmp_ne_u32_e64 s[16:17], 1, v2
	s_cbranch_vccnz .LBB1_171
	global_store_dwordx2 v[172:173], v[18:19], off
	s_or_b32 s70, s40, 1
	s_and_saveexec_b64 s[68:69], s[12:13]
	v_mov_b32_e32 v3, s70
	global_store_dword v[174:175], v3, off
	s_mov_b64 exec, s[68:69]
	s_cbranch_execnz .LBB1_109
.LBB1_108:
	global_store_dwordx2 v[172:173], v[18:19], off sc1
	s_or_b32 s70, s40, 1
	s_and_saveexec_b64 s[68:69], s[12:13]
	v_mov_b32_e32 v3, s70
	global_store_dword v[174:175], v3, off sc1
	s_mov_b64 exec, s[68:69]
.LBB1_109:
	v_accvgpr_read_b32 v0, a0
	v_accvgpr_read_b32 v1, a1
	v_accvgpr_read_b32 v2, a2
	v_accvgpr_read_b32 v3, a3
	v_fma_mixlo_f16 v18, v20, v24, 0
	v_fma_mixlo_f16 v19, v21, v25, 0
	v_fma_mixlo_f16 v20, v22, v26, 0
	v_fma_mixlo_f16 v21, v23, v27, 0
	v_mul_f32_e32 v10, v255, v10
	v_fmac_f32_e32 v10, v254, v6
	v_add_f32_e32 v0, v252, v0
	v_fmac_f32_e32 v10, v253, v14
	v_add_f32_e32 v0, v0, v10
	v_mul_f32_e32 v0, 0xbfb8aa3b, v0
	v_exp_f32_e32 v0, v0
	v_mul_f32_e32 v6, v255, v11
	v_fmac_f32_e32 v6, v254, v7
	v_add_f32_e32 v1, v252, v1
	v_fmac_f32_e32 v6, v253, v15
	v_add_f32_e32 v1, v1, v6
	v_add_f32_e32 v0, 1.0, v0
	v_mul_f32_e32 v1, 0xbfb8aa3b, v1
	v_rcp_f32_e32 v0, v0
	v_exp_f32_e32 v1, v1
	ds_write_b32 v184, v0 offset:29696
	ds_write_b16 v247, v18 offset:12800
	v_add_f32_e32 v0, 1.0, v1
	v_add_f32_e32 v1, v252, v2
	v_mul_f32_e32 v2, v255, v12
	v_fmac_f32_e32 v2, v254, v8
	v_fmac_f32_e32 v2, v253, v16
	v_add_f32_e32 v1, v1, v2
	v_add_f32_e32 v2, v252, v3
	v_mul_f32_e32 v3, v255, v13
	v_fmac_f32_e32 v3, v254, v9
	v_mul_f32_e32 v1, 0xbfb8aa3b, v1
	v_fmac_f32_e32 v3, v253, v17
	v_rcp_f32_e32 v0, v0
	v_exp_f32_e32 v1, v1
	v_add_f32_e32 v2, v2, v3
	v_mul_f32_e32 v2, 0xbfb8aa3b, v2
	v_exp_f32_e32 v2, v2
	ds_write_b32 v250, v0 offset:29696
	v_add_f32_e32 v0, 1.0, v1
	v_rcp_f32_e32 v0, v0
	v_add_f32_e32 v1, 1.0, v2
	v_rcp_f32_e32 v1, v1
	ds_write_b16 v247, v19 offset:13344
	ds_write_b32 v185, v0 offset:29696
	ds_write_b16 v247, v20 offset:13888
	ds_write_b32 v251, v1 offset:29696
	ds_write_b16 v247, v21 offset:14432
	s_xor_b64 s[30:31], s[30:31], -1
	s_andn2_b64 vcc, exec, s[30:31]
	s_mov_b64 s[30:31], -1
	s_add_i32 s71, s40, 1
	global_load_dword v50, v[168:169], off sc1
	s_waitcnt lgkmcnt(0)
	s_barrier
	ds_read_b128 v[54:57], v208 offset:34832
	ds_read_b128 v[64:67], v208 offset:48144
	ds_read_b128 v[68:71], v209 offset:34832
	ds_read_b128 v[72:75], v209 offset:48144
	ds_read_b128 v[78:81], v210 offset:34832
	ds_read_b128 v[82:85], v210 offset:48144
	ds_read_b128 v[86:89], v211 offset:34832
	ds_read_b128 v[90:93], v211 offset:48144
	ds_read_b128 v[94:97], v212 offset:34832
	ds_read_b128 v[98:101], v212 offset:48144
	ds_read_b128 v[102:105], v213 offset:34832
	ds_read_b128 v[106:109], v213 offset:48144
	ds_read_b128 v[114:117], v214 offset:34832
	ds_read_b128 v[118:121], v214 offset:48144
	ds_read_b128 v[122:125], v215 offset:34832
	ds_read_b128 v[126:129], v215 offset:48144
	ds_read_b128 v[130:133], v216 offset:34832
	ds_read_b128 v[134:137], v216 offset:48144
	ds_read_b128 v[138:141], v217 offset:34832
	ds_read_b128 v[142:145], v217 offset:48144
	ds_read_b128 v[146:149], v218 offset:34832
	ds_read_b128 v[150:153], v218 offset:48144
	ds_read_b128 v[154:157], v219 offset:34832
	ds_read_b128 v[158:161], v219 offset:48144
	ds_read_b128 v[162:165], v220 offset:34832
	ds_read_b128 v[180:183], v220 offset:48144
	global_load_dword v51, v[168:169], off sc1
.Lpl1_loop:
	s_waitcnt vmcnt(1)
	v_cmp_le_u32_e64 s[66:67], s71, v50
	s_cmp_eq_u64 s[66:67], exec
	s_cbranch_scc1 .Lpl1_done
	s_waitcnt vmcnt(0)
	v_cmp_le_u32_e64 s[66:67], s71, v51
	s_cmp_eq_u64 s[66:67], exec
	s_cbranch_scc1 .Lpl1_done
	s_add_i32 s65, s65, 1
	s_cmp_gt_u32 s65, 0xffff
	s_cbranch_scc1 .Lpl1_done
	global_load_dword v50, v[168:169], off sc1
	s_sleep 2
	global_load_dword v51, v[168:169], off sc1
	s_branch .Lpl1_loop
.Lpl1_done:
.LBB1_123:
	buffer_load_dwordx4 v[0:3], v229, s[20:23], 0 offen sc1
	buffer_load_dwordx4 v[6:9], v230, s[20:23], 0 offen sc1
	buffer_load_dwordx4 v[10:13], v231, s[20:23], 0 offen sc1
	buffer_load_dwordx4 v[14:17], v232, s[20:23], 0 offen sc1
	buffer_load_dwordx4 v[18:21], v233, s[20:23], 0 offen sc1
	buffer_load_dwordx4 v[22:25], v234, s[20:23], 0 offen sc1
	buffer_load_dwordx4 v[26:29], v235, s[20:23], 0 offen sc1
	buffer_load_dwordx4 v[30:33], v236, s[20:23], 0 offen sc1
	s_load_dwordx2 s[36:37], s[34:35], 0x20
	s_or_b32 s26, s42, 1
	buffer_load_dwordx4 v[34:37], v237, s[20:23], 0 offen sc1
	buffer_load_dwordx4 v[38:41], v238, s[20:23], 0 offen sc1
	buffer_load_dwordx4 v[42:45], v239, s[20:23], 0 offen sc1
	buffer_load_dwordx4 v[46:49], v240, s[20:23], 0 offen sc1
	buffer_load_dwordx4 v[50:53], v241, s[20:23], 0 offen sc1
	s_mulk_i32 s26, 0x600
	v_lshl_add_u64 v[252:253], v[176:177], 0, s[26:27]
	s_waitcnt lgkmcnt(0)
	global_load_dword v186, v110, s[36:37]
	global_load_dword v190, v[252:253], off
	global_load_dword v191, v[252:253], off offset:512
	global_load_dword v192, v[252:253], off offset:1024
	s_mov_b64 s[36:37], -1
.Ltg1_entry:
	v_mov_b32_e32 v255, 0
	s_waitcnt vmcnt(16) lgkmcnt(14)
	v_xor_b32_e32 v1, s64, v1
	v_xor_b32_e32 v3, s64, v3
	v_or3_b32 v255, v255, v1, v3
	s_nop 0
	v_mfma_f32_16x16x32_f16 a[0:3], v[0:3], v[54:57], 0
	v_mfma_f32_16x16x32_f16 a[4:7], v[0:3], v[64:67], 0
	s_waitcnt vmcnt(15)
	v_xor_b32_e32 v7, s64, v7
	v_xor_b32_e32 v9, s64, v9
	v_or3_b32 v255, v255, v7, v9
	s_nop 0
	v_mfma_f32_16x16x32_f16 a[0:3], v[6:9], v[68:71], a[0:3]
	v_mfma_f32_16x16x32_f16 a[4:7], v[6:9], v[72:75], a[4:7]
	s_waitcnt vmcnt(14)
	v_xor_b32_e32 v11, s64, v11
	v_xor_b32_e32 v13, s64, v13
	v_or3_b32 v255, v255, v11, v13
	s_nop 0
	v_mfma_f32_16x16x32_f16 a[0:3], v[10:13], v[78:81], a[0:3]
	v_mfma_f32_16x16x32_f16 a[4:7], v[10:13], v[82:85], a[4:7]
	s_waitcnt vmcnt(13)
	v_xor_b32_e32 v15, s64, v15
	v_xor_b32_e32 v17, s64, v17
	v_or3_b32 v255, v255, v15, v17
	s_nop 0
	v_mfma_f32_16x16x32_f16 a[0:3], v[14:17], v[86:89], a[0:3]
	v_mfma_f32_16x16x32_f16 a[4:7], v[14:17], v[90:93], a[4:7]
	s_waitcnt vmcnt(12)
	v_xor_b32_e32 v19, s64, v19
	v_xor_b32_e32 v21, s64, v21
	v_or3_b32 v255, v255, v19, v21
	s_nop 0
	v_mfma_f32_16x16x32_f16 a[0:3], v[18:21], v[94:97], a[0:3]
	v_mfma_f32_16x16x32_f16 a[4:7], v[18:21], v[98:101], a[4:7]
	s_waitcnt vmcnt(11)
	v_xor_b32_e32 v23, s64, v23
	v_xor_b32_e32 v25, s64, v25
	v_or3_b32 v255, v255, v23, v25
	s_nop 0
	v_mfma_f32_16x16x32_f16 a[0:3], v[22:25], v[102:105], a[0:3]
	v_mfma_f32_16x16x32_f16 a[4:7], v[22:25], v[106:109], a[4:7]
	s_waitcnt vmcnt(10) lgkmcnt(13)
	v_xor_b32_e32 v27, s64, v27
	v_xor_b32_e32 v29, s64, v29
	v_or3_b32 v255, v255, v27, v29
	s_nop 0
	v_mfma_f32_16x16x32_f16 a[0:3], v[26:29], v[114:117], a[0:3]
	s_waitcnt lgkmcnt(12)
	v_mfma_f32_16x16x32_f16 a[4:7], v[26:29], v[118:121], a[4:7]
	s_waitcnt vmcnt(9) lgkmcnt(11)
	v_xor_b32_e32 v31, s64, v31
	v_xor_b32_e32 v33, s64, v33
	v_or3_b32 v255, v255, v31, v33
	s_nop 0
	v_mfma_f32_16x16x32_f16 a[0:3], v[30:33], v[122:125], a[0:3]
	s_waitcnt lgkmcnt(10)
	v_mfma_f32_16x16x32_f16 a[4:7], v[30:33], v[126:129], a[4:7]
	s_waitcnt vmcnt(8) lgkmcnt(9)
	v_xor_b32_e32 v35, s64, v35
	v_xor_b32_e32 v37, s64, v37
	v_or3_b32 v255, v255, v35, v37
	s_nop 0
	v_mfma_f32_16x16x32_f16 a[0:3], v[34:37], v[130:133], a[0:3]
	s_waitcnt lgkmcnt(8)
	v_mfma_f32_16x16x32_f16 a[4:7], v[34:37], v[134:137], a[4:7]
	s_waitcnt vmcnt(7) lgkmcnt(7)
	v_xor_b32_e32 v39, s64, v39
	v_xor_b32_e32 v41, s64, v41
	v_or3_b32 v255, v255, v39, v41
	s_nop 0
	v_mfma_f32_16x16x32_f16 a[0:3], v[38:41], v[138:141], a[0:3]
	s_waitcnt lgkmcnt(6)
	v_mfma_f32_16x16x32_f16 a[4:7], v[38:41], v[142:145], a[4:7]
	s_waitcnt vmcnt(6) lgkmcnt(5)
	v_xor_b32_e32 v43, s64, v43
	v_xor_b32_e32 v45, s64, v45
	v_or3_b32 v255, v255, v43, v45
	s_nop 0
	v_mfma_f32_16x16x32_f16 a[0:3], v[42:45], v[146:149], a[0:3]
	s_waitcnt lgkmcnt(4)
	v_mfma_f32_16x16x32_f16 a[4:7], v[42:45], v[150:153], a[4:7]
	s_waitcnt vmcnt(5) lgkmcnt(3)
	v_xor_b32_e32 v47, s64, v47
	v_xor_b32_e32 v49, s64, v49
	v_or3_b32 v255, v255, v47, v49
	s_nop 0
	v_mfma_f32_16x16x32_f16 a[0:3], v[46:49], v[154:157], a[0:3]
	s_waitcnt vmcnt(4) lgkmcnt(1)
	v_xor_b32_e32 v51, s64, v51
	v_xor_b32_e32 v53, s64, v53
	v_or3_b32 v255, v255, v51, v53
	s_nop 0
	v_mfma_f32_16x16x32_f16 a[0:3], v[50:53], v[162:165], a[0:3]
	v_mfma_f32_16x16x32_f16 a[4:7], v[46:49], v[158:161], a[4:7]
	v_and_b32_e32 v255, s64, v255
	v_cmp_ne_u32_e64 s[66:67], 0, v255
	s_cmp_lg_u64 s[66:67], 0
	s_cbranch_scc1 .Ltg1_redo
.Ltg1_go:
	s_nop 2
	v_accvgpr_read_b32 v0, a0
	v_accvgpr_read_b32 v2, a1
	v_accvgpr_read_b32 v1, a2
	v_accvgpr_read_b32 v3, a3
	s_waitcnt lgkmcnt(0)
	v_mfma_f32_16x16x32_f16 a[0:3], v[50:53], v[180:183], a[4:7]
	v_cvt_pk_f16_f32 v1, v1, v3
	v_cvt_pk_f16_f32 v0, v0, v2
	v_add_u32_e32 v182, v111, v207
	s_nop 4
	v_accvgpr_read_b32 v2, a0
	v_accvgpr_read_b32 v6, a1
	v_accvgpr_read_b32 v3, a2
	v_accvgpr_read_b32 v7, a3
	v_cvt_pk_f16_f32 v3, v3, v7
	v_cvt_pk_f16_f32 v2, v2, v6
	ds_write2_b64 v248, v[0:1], v[2:3] offset0:80 offset1:96
	s_waitcnt lgkmcnt(0)
	s_barrier
	ds_read_b128 v[0:3], v182 offset:12800
	ds_read_b128 v[6:9], v182 offset:12864
	ds_read_b128 v[10:13], v182 offset:12928
	ds_read_b128 v[14:17], v182 offset:12992
	ds_read_b128 v[18:21], v182 offset:13056
	ds_read_b128 v[22:25], v182 offset:13120
	ds_read2st64_b32 v[42:43], v242 offset0:84 offset1:116
	ds_read_b128 v[38:41], v225 offset:33792
	ds_read_b128 v[26:29], v225 offset:33856
	ds_read_b128 v[30:33], v225 offset:33920
	v_or_b32_e32 v36, v110, v227
	v_or_b32_e32 v34, v110, v226
	ds_read2st64_b32 v[44:45], v36 offset0:84 offset1:116
	v_or_b32_e32 v36, v110, v228
	ds_read2st64_b32 v[34:35], v34 offset0:84 offset1:116
	ds_read2st64_b32 v[36:37], v36 offset0:84 offset1:116
	s_waitcnt lgkmcnt(12)
	v_mfma_f32_16x16x32_f16 a[0:3], v[0:3], a[56:59], 0
	s_waitcnt lgkmcnt(11)
	v_mfma_f32_16x16x32_f16 a[0:3], v[6:9], a[60:63], a[0:3]
	s_waitcnt lgkmcnt(10)
	v_mfma_f32_16x16x32_f16 a[0:3], v[10:13], a[64:67], a[0:3]
	s_waitcnt lgkmcnt(9)
	v_mfma_f32_16x16x32_f16 a[0:3], v[14:17], a[68:71], a[0:3]
	s_waitcnt lgkmcnt(8)
	v_mfma_f32_16x16x32_f16 a[0:3], v[18:21], a[72:75], a[0:3]
	s_waitcnt lgkmcnt(7)
	v_mfma_f32_16x16x32_f16 a[0:3], v[22:25], a[76:79], a[0:3]
	s_nop 7
	v_accvgpr_read_b32 v7, a1
	v_accvgpr_read_b32 v9, a0
	v_accvgpr_read_b32 v1, a3
	v_accvgpr_read_b32 v3, a2
	s_waitcnt lgkmcnt(5)
	v_mov_b32_e32 v10, v38
	s_waitcnt lgkmcnt(4)
	v_mov_b32_e32 v11, v26
	s_waitcnt vmcnt(1)
	v_mul_f32_e32 v0, v191, v26
	v_pk_fma_f32 v[10:11], v[190:191], v[10:11], v[0:1] op_sel_hi:[1,1,0]
	s_waitcnt vmcnt(0) lgkmcnt(3)
	v_mul_f32_e32 v8, v192, v30
	v_mov_b32_e32 v11, v186
	v_pk_add_f32 v[8:9], v[10:11], v[8:9]
	v_mov_b32_e32 v26, v39
	v_add_f32_e32 v0, v8, v9
	v_mul_f32_e32 v0, 0x4038aa3b, v0
	v_exp_f32_e32 v2, v0
	v_mul_f32_e32 v0, v191, v27
	v_pk_fma_f32 v[8:9], v[190:191], v[26:27], v[0:1] op_sel_hi:[1,1,0]
	v_mul_f32_e32 v6, v192, v31
	v_mov_b32_e32 v9, v186
	v_pk_add_f32 v[6:7], v[8:9], v[6:7]
	v_mov_b32_e32 v10, v40
	v_add_f32_e32 v0, v6, v7
	v_mul_f32_e32 v0, 0x4038aa3b, v0
	v_exp_f32_e32 v0, v0
	v_mov_b32_e32 v11, v28
	v_add_f32_e32 v2, 1.0, v2
	v_rcp_f32_e32 v6, v2
	v_add_f32_e32 v0, 1.0, v0
	v_rcp_f32_e32 v7, v0
	v_mul_f32_e32 v0, v191, v28
	v_pk_fma_f32 v[10:11], v[190:191], v[10:11], v[0:1] op_sel_hi:[1,1,0]
	v_mul_f32_e32 v2, v192, v32
	v_mov_b32_e32 v11, v186
	v_pk_add_f32 v[2:3], v[10:11], v[2:3]
	v_mov_b32_e32 v28, v41
	v_add_f32_e32 v0, v2, v3
	v_mul_f32_e32 v2, v191, v29
	v_mul_f32_e32 v0, 0x4038aa3b, v0
	v_pk_fma_f32 v[2:3], v[190:191], v[28:29], v[2:3] op_sel_hi:[1,1,0]
	v_exp_f32_e32 v10, v0
	v_mul_f32_e32 v0, v192, v33
	v_mov_b32_e32 v3, v186
	v_pk_add_f32 v[0:1], v[2:3], v[0:1]
	v_add_f32_e32 v2, 1.0, v10
	v_add_f32_e32 v0, v0, v1
	v_mul_f32_e32 v0, 0x4038aa3b, v0
	v_exp_f32_e32 v3, v0
	v_rcp_f32_e32 v2, v2
	s_waitcnt lgkmcnt(1)
	v_mov_b32_e32 v9, v34
	v_mov_b32_e32 v34, v43
	v_add_f32_e32 v3, 1.0, v3
	v_rcp_f32_e32 v3, v3
	v_pk_fma_f32 v[6:7], v[6:7], 2.0, 1.0 op_sel_hi:[1,0,0] neg_lo:[1,0,0] neg_hi:[1,0,0]
	v_pk_add_f32 v[0:1], v[34:35], 1.0 op_sel_hi:[1,0] neg_lo:[1,0] neg_hi:[1,0]
	v_mov_b32_e32 v8, v42
	v_pk_mul_f32 v[0:1], v[0:1], v[6:7]
	s_and_b64 vcc, exec, s[16:17]
	v_pk_fma_f32 v[8:9], v[8:9], v[34:35], v[0:1]
	v_pk_fma_f32 v[0:1], v[2:3], 2.0, 1.0 op_sel_hi:[1,0,0] neg_lo:[1,0,0] neg_hi:[1,0,0]
	s_waitcnt lgkmcnt(0)
	v_mov_b32_e32 v3, v36
	v_mov_b32_e32 v36, v45
	v_pk_add_f32 v[10:11], v[36:37], 1.0 op_sel_hi:[1,0] neg_lo:[1,0] neg_hi:[1,0]
	v_mov_b32_e32 v2, v44
	v_pk_mul_f32 v[0:1], v[10:11], v[0:1]
	v_cvt_pk_f16_f32 v6, v8, v9
	v_pk_fma_f32 v[10:11], v[2:3], v[36:37], v[0:1]
	s_nop 0
	v_cvt_pk_f16_f32 v7, v10, v11
	v_mov_b32_e32 v2, v6
	v_or_b32_e32 v3, s64, v7
	s_cbranch_vccnz .LBB1_125
	s_mov_b64 s[36:37], 0
	global_store_dwordx2 v[178:179], v[2:3], off
	s_or_b32 s70, s40, 2
	s_and_saveexec_b64 s[68:69], s[12:13]
	v_mov_b32_e32 v0, s70
	global_store_dword v[174:175], v0, off
	s_mov_b64 exec, s[68:69]
.LBB1_125:
	s_andn2_b64 vcc, exec, s[36:37]
	s_cbranch_vccnz .LBB1_127
	global_store_dwordx2 v[178:179], v[2:3], off sc1
	s_or_b32 s70, s40, 2
	s_and_saveexec_b64 s[68:69], s[12:13]
	v_mov_b32_e32 v0, s70
	global_store_dword v[174:175], v0, off sc1
	s_mov_b64 exec, s[68:69]
.LBB1_127:
	s_or_b32 s26, s40, 2
	ds_write_b32 v184, v8 offset:21504
	ds_write_b16 v245, v6
	ds_write_b32 v250, v9 offset:21504
	ds_write_b16_d16_hi v245, v6 offset:800
	ds_write_b32 v185, v10 offset:21504
	ds_write_b16 v245, v7 offset:1600
	ds_write_b32 v251, v11 offset:21504
	ds_write_b16_d16_hi v245, v7 offset:2400
	s_xor_b64 s[30:31], s[30:31], -1
	s_andn2_b64 vcc, exec, s[30:31]
	s_mov_b64 s[30:31], -1
	s_add_i32 s71, s40, 2
	global_load_dword v50, v[168:169], off sc1
	s_waitcnt lgkmcnt(0)
	s_barrier
	ds_read_b128 v[54:57], v58 offset:4096
	ds_read_b128 v[64:67], v58 offset:5120
	ds_read_b128 v[68:71], v249 offset:128
	ds_read_b128 v[72:75], v249 offset:192
	ds_read_b128 v[78:81], v58 offset:6144
	ds_read_b128 v[82:85], v58 offset:7168
	ds_read_b128 v[86:89], v58 offset:12288
	ds_read_b128 v[90:93], v58 offset:13312
	ds_read_b128 v[94:97], v249 offset:384
	ds_read_b128 v[98:101], v249 offset:448
	ds_read_b128 v[102:105], v58 offset:14336
	ds_read_b128 v[106:109], v58 offset:15360
	ds_read_b128 v[114:117], v58 offset:20480
	ds_read_b128 v[118:121], v58 offset:21504
	ds_read_b128 v[122:125], v249 offset:640
	ds_read_b128 v[126:129], v249 offset:704
	ds_read_b128 v[130:133], v58 offset:22528
	ds_read_b128 v[134:137], v58 offset:23552
	s_waitcnt lgkmcnt(14)
	v_mfma_f32_16x16x32_f16 a[0:3], v[68:71], v[54:57], 0
	s_waitcnt lgkmcnt(13)
	v_mfma_f32_16x16x32_f16 a[0:3], v[72:75], v[78:81], a[0:3]
	s_waitcnt lgkmcnt(9)
	v_mfma_f32_16x16x32_f16 a[0:3], v[94:97], v[86:89], a[0:3]
	s_waitcnt lgkmcnt(7)
	v_mfma_f32_16x16x32_f16 a[0:3], v[98:101], v[102:105], a[0:3]
	s_waitcnt lgkmcnt(3)
	v_mfma_f32_16x16x32_f16 a[0:3], v[122:125], v[114:117], a[0:3]
	s_waitcnt lgkmcnt(1)
	v_mfma_f32_16x16x32_f16 a[4:7], v[126:129], v[130:133], a[0:3]
	v_mfma_f32_16x16x32_f16 a[0:3], v[68:71], v[64:67], 0
	v_mfma_f32_16x16x32_f16 a[0:3], v[72:75], v[82:85], a[0:3]
	v_mfma_f32_16x16x32_f16 a[0:3], v[94:97], v[90:93], a[0:3]
	v_mfma_f32_16x16x32_f16 a[0:3], v[98:101], v[106:109], a[0:3]
	v_mfma_f32_16x16x32_f16 a[0:3], v[122:125], v[118:121], a[0:3]
	s_waitcnt lgkmcnt(0)
	v_mfma_f32_16x16x32_f16 a[0:3], v[126:129], v[134:137], a[0:3]
	global_load_dword v51, v[168:169], off sc1

.Lpl2_done:
.LBB1_141:
	buffer_load_dwordx4 v[0:3], v194, s[20:23], 0 offen sc1
	buffer_load_dwordx4 v[6:9], v195, s[20:23], 0 offen sc1
	buffer_load_dwordx4 v[10:13], v196, s[20:23], 0 offen sc1
	buffer_load_dwordx4 v[14:17], v197, s[20:23], 0 offen sc1
	buffer_load_dwordx4 v[18:21], v198, s[20:23], 0 offen sc1
	buffer_load_dwordx4 v[22:25], v199, s[20:23], 0 offen sc1
	buffer_load_dwordx4 v[26:29], v200, s[20:23], 0 offen sc1
	buffer_load_dwordx4 v[30:33], v201, s[20:23], 0 offen sc1
	s_load_dwordx2 s[36:37], s[34:35], 0x28
	buffer_load_dwordx4 v[34:37], v202, s[20:23], 0 offen sc1
	buffer_load_dwordx4 v[38:41], v203, s[20:23], 0 offen sc1
	buffer_load_dwordx4 v[42:45], v204, s[20:23], 0 offen sc1
	buffer_load_dwordx4 v[46:49], v205, s[20:23], 0 offen sc1
	buffer_load_dwordx4 v[50:53], v206, s[20:23], 0 offen sc1
	s_waitcnt lgkmcnt(0)
	global_load_dword v180, v110, s[36:37]
	global_load_dword v183, v110, s[36:37] offset:256
	s_mov_b64 s[36:37], -1
	ds_read_b128 v[54:57], v208 offset:34832
	ds_read_b128 v[64:67], v208 offset:48144
	ds_read_b128 v[68:71], v209 offset:34832
	ds_read_b128 v[72:75], v209 offset:48144
	ds_read_b128 v[78:81], v210 offset:34832
	ds_read_b128 v[82:85], v210 offset:48144
	ds_read_b128 v[86:89], v211 offset:34832
	ds_read_b128 v[90:93], v211 offset:48144
	ds_read_b128 v[94:97], v212 offset:34832
	ds_read_b128 v[98:101], v212 offset:48144
	ds_read_b128 v[102:105], v213 offset:34832
	ds_read_b128 v[106:109], v213 offset:48144
	ds_read_b128 v[114:117], v214 offset:34832
	ds_read_b128 v[118:121], v214 offset:48144
	ds_read_b128 v[122:125], v215 offset:34832
	ds_read_b128 v[126:129], v215 offset:48144
	ds_read_b128 v[130:133], v216 offset:34832
	ds_read_b128 v[134:137], v216 offset:48144
	ds_read_b128 v[138:141], v217 offset:34832
	ds_read_b128 v[142:145], v217 offset:48144
	ds_read_b128 v[146:149], v218 offset:34832
	ds_read_b128 v[150:153], v218 offset:48144
	ds_read_b128 v[154:157], v219 offset:34832
	ds_read_b128 v[158:161], v219 offset:48144
	ds_read_b128 v[162:165], v220 offset:34832
	ds_read_b128 v[190:193], v220 offset:48144
.Ltg2_entry:
	v_mov_b32_e32 v255, 0
	s_waitcnt vmcnt(14) lgkmcnt(14)
	v_xor_b32_e32 v1, s64, v1
	v_xor_b32_e32 v3, s64, v3
	v_or3_b32 v255, v255, v1, v3
	s_nop 0
	v_mfma_f32_16x16x32_f16 a[128:131], v[0:3], v[54:57], 0
	v_mfma_f32_16x16x32_f16 a[132:135], v[0:3], v[64:67], 0
	s_waitcnt vmcnt(13)
	v_xor_b32_e32 v7, s64, v7
	v_xor_b32_e32 v9, s64, v9
	v_or3_b32 v255, v255, v7, v9
	s_nop 0
	v_mfma_f32_16x16x32_f16 a[128:131], v[6:9], v[68:71], a[128:131]
	v_mfma_f32_16x16x32_f16 a[132:135], v[6:9], v[72:75], a[132:135]
	s_waitcnt vmcnt(12)
	v_xor_b32_e32 v11, s64, v11
	v_xor_b32_e32 v13, s64, v13
	v_or3_b32 v255, v255, v11, v13
	s_nop 0
	v_mfma_f32_16x16x32_f16 a[128:131], v[10:13], v[78:81], a[128:131]
	v_mfma_f32_16x16x32_f16 a[132:135], v[10:13], v[82:85], a[132:135]
	s_waitcnt vmcnt(11)
	v_xor_b32_e32 v15, s64, v15
	v_xor_b32_e32 v17, s64, v17
	v_or3_b32 v255, v255, v15, v17
	s_nop 0
	v_mfma_f32_16x16x32_f16 a[128:131], v[14:17], v[86:89], a[128:131]
	v_mfma_f32_16x16x32_f16 a[132:135], v[14:17], v[90:93], a[132:135]
	ds_read_b128 v[0:3], v187 offset:61456
	ds_read_b128 v[10:13], v187 offset:62480
	ds_read_b128 v[64:67], v187 offset:63504
	ds_read_b128 v[14:17], v187 offset:64528
	s_waitcnt vmcnt(10)
	v_xor_b32_e32 v19, s64, v19
	v_xor_b32_e32 v21, s64, v21
	v_or3_b32 v255, v255, v19, v21
	s_nop 0
	v_mfma_f32_16x16x32_f16 a[128:131], v[18:21], v[94:97], a[128:131]
	v_mfma_f32_16x16x32_f16 a[132:135], v[18:21], v[98:101], a[132:135]
	s_waitcnt vmcnt(9)
	v_xor_b32_e32 v23, s64, v23
	v_xor_b32_e32 v25, s64, v25
	v_or3_b32 v255, v255, v23, v25
	s_nop 0
	v_mfma_f32_16x16x32_f16 a[128:131], v[22:25], v[102:105], a[128:131]
	v_mfma_f32_16x16x32_f16 a[132:135], v[22:25], v[106:109], a[132:135]
	ds_read_b128 v[68:71], v188 offset:8192
	ds_read_b128 v[18:21], v188 offset:9216
	ds_read_b128 v[72:75], v188 offset:10240
	ds_read_b128 v[22:25], v188 offset:11264
	s_waitcnt vmcnt(8) lgkmcnt(14)
	v_xor_b32_e32 v27, s64, v27
	v_xor_b32_e32 v29, s64, v29
	v_or3_b32 v255, v255, v27, v29
	s_nop 0
	v_mfma_f32_16x16x32_f16 a[128:131], v[26:29], v[114:117], a[128:131]
	v_mfma_f32_16x16x32_f16 a[132:135], v[26:29], v[118:121], a[132:135]
	ds_read_b128 v[78:81], v188 offset:16384
	ds_read_b128 v[26:29], v188 offset:17408
	ds_read_b128 v[82:85], v188 offset:18432
	ds_read_b128 v[6:9], v188 offset:19456
	s_waitcnt vmcnt(7)
	v_xor_b32_e32 v31, s64, v31
	v_xor_b32_e32 v33, s64, v33
	v_or3_b32 v255, v255, v31, v33
	s_nop 0
	v_mfma_f32_16x16x32_f16 a[128:131], v[30:33], v[122:125], a[128:131]
	v_mfma_f32_16x16x32_f16 a[132:135], v[30:33], v[126:129], a[132:135]
	s_waitcnt vmcnt(6)
	v_xor_b32_e32 v35, s64, v35
	v_xor_b32_e32 v37, s64, v37
	v_or3_b32 v255, v255, v35, v37
	s_nop 0
	v_mfma_f32_16x16x32_f16 a[128:131], v[34:37], v[130:133], a[128:131]
	v_mfma_f32_16x16x32_f16 a[132:135], v[34:37], v[134:137], a[132:135]
	s_waitcnt vmcnt(5)
	v_xor_b32_e32 v39, s64, v39
	v_xor_b32_e32 v41, s64, v41
	v_or3_b32 v255, v255, v39, v41
	s_nop 0
	v_mfma_f32_16x16x32_f16 a[128:131], v[38:41], v[138:141], a[128:131]
	v_mfma_f32_16x16x32_f16 a[132:135], v[38:41], v[142:145], a[132:135]
	s_waitcnt vmcnt(4) lgkmcnt(14)
	v_xor_b32_e32 v43, s64, v43
	v_xor_b32_e32 v45, s64, v45
	v_or3_b32 v255, v255, v43, v45
	s_nop 0
	v_mfma_f32_16x16x32_f16 a[128:131], v[42:45], v[146:149], a[128:131]
	v_mfma_f32_16x16x32_f16 a[132:135], v[42:45], v[150:153], a[132:135]
	s_waitcnt vmcnt(3)
	v_xor_b32_e32 v47, s64, v47
	v_xor_b32_e32 v49, s64, v49
	v_or3_b32 v255, v255, v47, v49
	s_nop 0
	v_mfma_f32_16x16x32_f16 a[128:131], v[46:49], v[154:157], a[128:131]
	s_waitcnt vmcnt(2) lgkmcnt(13)
	v_xor_b32_e32 v51, s64, v51
	v_xor_b32_e32 v53, s64, v53
	v_or3_b32 v255, v255, v51, v53
	s_nop 0
	v_mfma_f32_16x16x32_f16 a[128:131], v[50:53], v[162:165], a[128:131]
	v_mfma_f32_16x16x32_f16 a[132:135], v[46:49], v[158:161], a[132:135]
	v_and_b32_e32 v255, s64, v255
	v_cmp_ne_u32_e64 s[66:67], 0, v255
	s_cmp_lg_u64 s[66:67], 0
	s_cbranch_scc1 .Ltg2_redo
.Ltg2_go:
	s_nop 2
	v_accvgpr_read_b32 v30, a128
	v_accvgpr_read_b32 v32, a129
	v_accvgpr_read_b32 v31, a130
	v_accvgpr_read_b32 v33, a131
	s_waitcnt lgkmcnt(12)
	v_mfma_f32_16x16x32_f16 a[128:131], v[50:53], v[190:193], a[132:135]
	v_cvt_pk_f16_f32 v31, v31, v33
	v_cvt_pk_f16_f32 v30, v30, v32
	s_nop 5
	v_accvgpr_read_b32 v32, a128
	v_accvgpr_read_b32 v34, a129
	v_accvgpr_read_b32 v33, a130
	v_accvgpr_read_b32 v35, a131
	v_cvt_pk_f16_f32 v33, v33, v35
	v_cvt_pk_f16_f32 v32, v32, v34
	ds_write2_b64 v221, v[30:31], v[32:33] offset0:32 offset1:64
	s_waitcnt lgkmcnt(0)
	s_barrier
	ds_read_b128 v[34:37], v249
	ds_read_b128 v[38:41], v249 offset:64
	ds_read_b128 v[42:45], v249 offset:256
	ds_read_b128 v[46:49], v249 offset:320
	ds_read_b128 v[50:53], v249 offset:512
	ds_read_b128 v[30:33], v249 offset:576
	ds_read2st64_b32 v[56:57], v184 offset0:100 offset1:101
	ds_read2st64_b32 v[54:55], v184 offset0:102 offset1:103
	s_waitcnt lgkmcnt(7)
	v_mfma_f32_16x16x32_f16 a[4:7], v[34:37], v[0:3], a[4:7]
	s_waitcnt lgkmcnt(6)
	v_mfma_f32_16x16x32_f16 a[4:7], v[38:41], v[64:67], a[4:7]
	s_waitcnt lgkmcnt(5)
	v_mfma_f32_16x16x32_f16 a[4:7], v[42:45], v[68:71], a[4:7]
	s_waitcnt lgkmcnt(4)
	v_mfma_f32_16x16x32_f16 a[4:7], v[46:49], v[72:75], a[4:7]
	s_waitcnt lgkmcnt(3)
	v_mfma_f32_16x16x32_f16 a[4:7], v[50:53], v[78:81], a[4:7]
	s_waitcnt lgkmcnt(2)
	v_mfma_f32_16x16x32_f16 a[4:7], v[30:33], v[82:85], a[4:7]
	s_nop 7
	v_accvgpr_read_b32 v0, a4
	s_waitcnt vmcnt(0)
	v_add_f32_e32 v0, v180, v0
	v_accvgpr_read_b32 v1, a5
	v_mul_f32_e32 v0, 0xbfb8aa3b, v0
	v_add_f32_e32 v1, v180, v1
	v_exp_f32_e32 v0, v0
	v_mul_f32_e32 v1, 0xbfb8aa3b, v1
	v_exp_f32_e32 v1, v1
	v_accvgpr_read_b32 v2, a7
	v_add_f32_e32 v0, 1.0, v0
	v_rcp_f32_e32 v186, v0
	v_add_f32_e32 v0, 1.0, v1
	v_accvgpr_read_b32 v1, a6
	v_add_f32_e32 v1, v180, v1
	v_mul_f32_e32 v1, 0xbfb8aa3b, v1
	v_add_f32_e32 v2, v180, v2
	v_exp_f32_e32 v1, v1
	v_mul_f32_e32 v2, 0xbfb8aa3b, v2
	v_exp_f32_e32 v2, v2
	v_rcp_f32_e32 v252, v0
	v_add_f32_e32 v0, 1.0, v1
	v_rcp_f32_e32 v253, v0
	v_add_f32_e32 v0, 1.0, v2
	v_rcp_f32_e32 v254, v0
	s_waitcnt lgkmcnt(1)
	v_mul_f32_e32 v0, v56, v186
	v_mul_f32_e32 v1, v57, v252
	s_waitcnt lgkmcnt(0)
	v_mul_f32_e32 v2, v54, v253
	v_mul_f32_e32 v3, v55, v254
	v_cvt_pk_f16_f32 v181, v2, v3
	s_and_b64 vcc, exec, s[16:17]
	v_cvt_pk_f16_f32 v180, v0, v1
	s_cbranch_vccnz .LBB1_143
	s_mov_b64 s[36:37], 0
	global_store_dwordx2 v[172:173], v[180:181], off
	s_or_b32 s70, s40, 3
	s_and_saveexec_b64 s[68:69], s[12:13]
	v_mov_b32_e32 v3, s70
	global_store_dword v[174:175], v3, off
	s_mov_b64 exec, s[68:69]
.LBB1_143:
	s_andn2_b64 vcc, exec, s[36:37]
	s_cbranch_vccnz .LBB1_145
	global_store_dwordx2 v[172:173], v[180:181], off sc1
	s_or_b32 s70, s40, 3
	s_and_saveexec_b64 s[68:69], s[12:13]
	v_mov_b32_e32 v3, s70
	global_store_dword v[174:175], v3, off sc1
	s_mov_b64 exec, s[68:69]
.LBB1_145:
	s_or_b32 s26, s40, 3
	v_fma_mixlo_f16 v0, v56, v186, 0
	v_fma_mixlo_f16 v1, v57, v252, 0
	v_fma_mixlo_f16 v2, v54, v253, 0
	v_fma_mixlo_f16 v3, v55, v254, 0
	v_mfma_f32_16x16x32_f16 a[0:3], v[34:37], v[10:13], a[0:3]
	ds_write_b16 v247, v0 offset:12800
	ds_write_b16 v247, v1 offset:13344
	ds_write_b16 v247, v2 offset:13888
	v_mfma_f32_16x16x32_f16 a[0:3], v[38:41], v[14:17], a[0:3]
	v_mfma_f32_16x16x32_f16 a[0:3], v[42:45], v[18:21], a[0:3]
	v_mfma_f32_16x16x32_f16 a[0:3], v[46:49], v[22:25], a[0:3]
	v_mfma_f32_16x16x32_f16 a[0:3], v[50:53], v[26:29], a[0:3]
	v_mfma_f32_16x16x32_f16 a[0:3], v[30:33], v[6:9], a[0:3]
	s_nop 7
	v_accvgpr_read_b32 v0, a0
	v_accvgpr_read_b32 v1, a1
	v_add_f32_e32 v0, v183, v0
	v_accvgpr_read_b32 v2, a2
	v_add_f32_e32 v1, v183, v1
	v_mul_f32_e32 v0, 0xbfb8aa3b, v0
	v_accvgpr_read_b32 v6, a3
	v_add_f32_e32 v2, v183, v2
	v_mul_f32_e32 v1, 0xbfb8aa3b, v1
	v_exp_f32_e32 v0, v0
	v_add_f32_e32 v6, v183, v6
	v_mul_f32_e32 v2, 0xbfb8aa3b, v2
	v_exp_f32_e32 v1, v1
	v_mul_f32_e32 v6, 0xbfb8aa3b, v6
	v_exp_f32_e32 v2, v2
	v_exp_f32_e32 v6, v6
	v_add_f32_e32 v0, 1.0, v0
	v_add_f32_e32 v1, 1.0, v1
	v_rcp_f32_e32 v0, v0
	v_add_f32_e32 v2, 1.0, v2
	v_rcp_f32_e32 v1, v1
	v_add_f32_e32 v6, 1.0, v6
	v_rcp_f32_e32 v2, v2
	v_rcp_f32_e32 v6, v6
	ds_write_b32 v184, v0 offset:29696
	ds_write_b32 v250, v1 offset:29696
	ds_write_b32 v185, v2 offset:29696
	ds_write_b32 v251, v6 offset:29696
	ds_write_b16 v247, v3 offset:14432
	s_xor_b64 s[30:31], s[30:31], -1
	s_andn2_b64 vcc, exec, s[30:31]
	s_mov_b64 s[30:31], -1
	s_add_i32 s71, s40, 3
	global_load_dword v50, v[168:169], off sc1
	s_waitcnt lgkmcnt(0)
	s_barrier
	ds_read_b128 v[54:57], v249
	ds_read_b128 v[64:67], v249 offset:64
	ds_read_b128 v[68:71], v249 offset:256
	ds_read_b128 v[72:75], v249 offset:320
	ds_read_b128 v[78:81], v249 offset:512
	ds_read_b128 v[82:85], v249 offset:576
	s_waitcnt lgkmcnt(5)
	v_mfma_f32_16x16x32_f16 a[0:3], v[54:57], a[80:83], 0
	s_waitcnt lgkmcnt(4)
	v_mfma_f32_16x16x32_f16 a[0:3], v[64:67], a[84:87], a[0:3]
	s_waitcnt lgkmcnt(3)
	v_mfma_f32_16x16x32_f16 a[0:3], v[68:71], a[96:99], a[0:3]
	s_waitcnt lgkmcnt(2)
	v_mfma_f32_16x16x32_f16 a[0:3], v[72:75], a[100:103], a[0:3]
	s_waitcnt lgkmcnt(1)
	v_mfma_f32_16x16x32_f16 a[0:3], v[78:81], a[112:115], a[0:3]
	s_waitcnt lgkmcnt(0)
	v_mfma_f32_16x16x32_f16 a[0:3], v[82:85], a[116:119], a[0:3]
	global_load_dword v51, v[168:169], off sc1

.Lpl3_done:
.LBB1_159:
	buffer_load_dwordx4 v[0:3], v229, s[20:23], 0 offen sc1
	buffer_load_dwordx4 v[6:9], v230, s[20:23], 0 offen sc1
	buffer_load_dwordx4 v[10:13], v231, s[20:23], 0 offen sc1
	buffer_load_dwordx4 v[14:17], v232, s[20:23], 0 offen sc1
	buffer_load_dwordx4 v[18:21], v233, s[20:23], 0 offen sc1
	buffer_load_dwordx4 v[22:25], v234, s[20:23], 0 offen sc1
	buffer_load_dwordx4 v[26:29], v235, s[20:23], 0 offen sc1
	buffer_load_dwordx4 v[30:33], v236, s[20:23], 0 offen sc1
	s_load_dwordx2 s[34:35], s[34:35], 0x30
	buffer_load_dwordx4 v[34:37], v237, s[20:23], 0 offen sc1
	buffer_load_dwordx4 v[38:41], v238, s[20:23], 0 offen sc1
	buffer_load_dwordx4 v[42:45], v239, s[20:23], 0 offen sc1
	buffer_load_dwordx4 v[46:49], v240, s[20:23], 0 offen sc1
	buffer_load_dwordx4 v[50:53], v241, s[20:23], 0 offen sc1
	s_waitcnt lgkmcnt(0)
	global_load_dword v180, v110, s[34:35]
	ds_read_b128 v[54:57], v208 offset:34832
	ds_read_b128 v[64:67], v208 offset:48144
	ds_read_b128 v[68:71], v209 offset:34832
	ds_read_b128 v[72:75], v209 offset:48144
	ds_read_b128 v[78:81], v210 offset:34832
	ds_read_b128 v[82:85], v210 offset:48144
	ds_read_b128 v[86:89], v211 offset:34832
	ds_read_b128 v[90:93], v211 offset:48144
	ds_read_b128 v[94:97], v212 offset:34832
	ds_read_b128 v[98:101], v212 offset:48144
	ds_read_b128 v[102:105], v213 offset:34832
	ds_read_b128 v[106:109], v213 offset:48144
	ds_read_b128 v[114:117], v214 offset:34832
	ds_read_b128 v[118:121], v214 offset:48144
	ds_read_b128 v[122:125], v215 offset:34832
	ds_read_b128 v[126:129], v215 offset:48144
	ds_read_b128 v[130:133], v216 offset:34832
	ds_read_b128 v[134:137], v216 offset:48144
	ds_read_b128 v[138:141], v217 offset:34832
	ds_read_b128 v[142:145], v217 offset:48144
	ds_read_b128 v[146:149], v218 offset:34832
	ds_read_b128 v[150:153], v218 offset:48144
	ds_read_b128 v[154:157], v219 offset:34832
	ds_read_b128 v[158:161], v219 offset:48144
	ds_read_b128 v[162:165], v220 offset:34832
	ds_read_b128 v[190:193], v220 offset:48144
.Ltg3_entry:
	v_mov_b32_e32 v255, 0
	s_waitcnt vmcnt(13) lgkmcnt(14)
	v_or3_b32 v255, v255, v1, v3
	v_mfma_f32_16x16x32_f16 a[4:7], v[0:3], v[54:57], 0
	v_mfma_f32_16x16x32_f16 a[128:131], v[0:3], v[64:67], 0
	s_waitcnt vmcnt(12)
	v_or3_b32 v255, v255, v7, v9
	v_mfma_f32_16x16x32_f16 a[4:7], v[6:9], v[68:71], a[4:7]
	v_mfma_f32_16x16x32_f16 a[128:131], v[6:9], v[72:75], a[128:131]
	s_waitcnt vmcnt(11)
	v_or3_b32 v255, v255, v11, v13
	v_mfma_f32_16x16x32_f16 a[4:7], v[10:13], v[78:81], a[4:7]
	v_mfma_f32_16x16x32_f16 a[128:131], v[10:13], v[82:85], a[128:131]
	s_waitcnt vmcnt(10)
	v_or3_b32 v255, v255, v15, v17
	v_mfma_f32_16x16x32_f16 a[4:7], v[14:17], v[86:89], a[4:7]
	v_mfma_f32_16x16x32_f16 a[128:131], v[14:17], v[90:93], a[128:131]
	s_waitcnt vmcnt(9)
	v_or3_b32 v255, v255, v19, v21
	v_mfma_f32_16x16x32_f16 a[4:7], v[18:21], v[94:97], a[4:7]
	v_mfma_f32_16x16x32_f16 a[128:131], v[18:21], v[98:101], a[128:131]
	s_waitcnt vmcnt(8)
	v_or3_b32 v255, v255, v23, v25
	v_mfma_f32_16x16x32_f16 a[4:7], v[22:25], v[102:105], a[4:7]
	v_mfma_f32_16x16x32_f16 a[128:131], v[22:25], v[106:109], a[128:131]
	s_waitcnt vmcnt(7) lgkmcnt(13)
	v_or3_b32 v255, v255, v27, v29
	v_mfma_f32_16x16x32_f16 a[4:7], v[26:29], v[114:117], a[4:7]
	s_waitcnt lgkmcnt(12)
	v_mfma_f32_16x16x32_f16 a[128:131], v[26:29], v[118:121], a[128:131]
	s_waitcnt vmcnt(6) lgkmcnt(11)
	v_or3_b32 v255, v255, v31, v33
	v_mfma_f32_16x16x32_f16 a[4:7], v[30:33], v[122:125], a[4:7]
	s_waitcnt lgkmcnt(10)
	v_mfma_f32_16x16x32_f16 a[128:131], v[30:33], v[126:129], a[128:131]
	s_waitcnt vmcnt(5) lgkmcnt(9)
	v_or3_b32 v255, v255, v35, v37
	v_mfma_f32_16x16x32_f16 a[4:7], v[34:37], v[130:133], a[4:7]
	s_waitcnt lgkmcnt(8)
	v_mfma_f32_16x16x32_f16 a[128:131], v[34:37], v[134:137], a[128:131]
	s_waitcnt vmcnt(4) lgkmcnt(7)
	v_or3_b32 v255, v255, v39, v41
	v_mfma_f32_16x16x32_f16 a[4:7], v[38:41], v[138:141], a[4:7]
	s_waitcnt lgkmcnt(6)
	v_mfma_f32_16x16x32_f16 a[128:131], v[38:41], v[142:145], a[128:131]
	s_waitcnt vmcnt(3) lgkmcnt(5)
	v_or3_b32 v255, v255, v43, v45
	v_mfma_f32_16x16x32_f16 a[4:7], v[42:45], v[146:149], a[4:7]
	s_waitcnt lgkmcnt(4)
	v_mfma_f32_16x16x32_f16 a[128:131], v[42:45], v[150:153], a[128:131]
	s_waitcnt vmcnt(2) lgkmcnt(3)
	v_or3_b32 v255, v255, v47, v49
	v_mfma_f32_16x16x32_f16 a[4:7], v[46:49], v[154:157], a[4:7]
	s_waitcnt vmcnt(1) lgkmcnt(1)
	v_or3_b32 v255, v255, v51, v53
	v_mfma_f32_16x16x32_f16 a[4:7], v[50:53], v[162:165], a[4:7]
	v_mfma_f32_16x16x32_f16 a[128:131], v[46:49], v[158:161], a[128:131]
	v_and_b32_e32 v255, s64, v255
	v_cmp_ne_u32_e64 s[66:67], 0, v255
	s_cmp_lg_u64 s[66:67], 0
	s_cbranch_scc1 .Ltg3_redo
.Ltg3_go:
	s_nop 2
	v_accvgpr_read_b32 v0, a4
	v_accvgpr_read_b32 v2, a5
	v_accvgpr_read_b32 v1, a6
	v_accvgpr_read_b32 v3, a7
	s_waitcnt lgkmcnt(0)
	v_mfma_f32_16x16x32_f16 a[4:7], v[50:53], v[190:193], a[128:131]
	v_cvt_pk_f16_f32 v1, v1, v3
	v_cvt_pk_f16_f32 v0, v0, v2
	s_nop 5
	v_accvgpr_read_b32 v2, a4
	v_accvgpr_read_b32 v6, a5
	v_accvgpr_read_b32 v3, a6
	v_accvgpr_read_b32 v7, a7
	v_cvt_pk_f16_f32 v3, v3, v7
	v_cvt_pk_f16_f32 v2, v2, v6
	ds_write2_b64 v221, v[0:1], v[2:3] offset0:48 offset1:80
	s_waitcnt lgkmcnt(0)
	s_barrier
	ds_read_b128 v[0:3], v182 offset:12800
	ds_read_b128 v[6:9], v182 offset:12864
	ds_read_b128 v[10:13], v249 offset:384
	ds_read_b128 v[14:17], v249 offset:448
	ds_read_b128 v[18:21], v249 offset:640
	ds_read_b128 v[22:25], v249 offset:704
	ds_read2st64_b32 v[26:27], v242 offset0:100 offset1:101
	ds_read2st64_b32 v[28:29], v242 offset0:116 offset1:117
	ds_read2st64_b32 v[30:31], v242 offset0:118 offset1:119
	ds_read2st64_b32 v[32:33], v242 offset0:102 offset1:103
	s_waitcnt lgkmcnt(9)
	v_mfma_f32_16x16x32_f16 a[0:3], v[0:3], a[88:91], a[0:3]
	s_waitcnt lgkmcnt(8)
	v_mfma_f32_16x16x32_f16 a[0:3], v[6:9], a[92:95], a[0:3]
	s_waitcnt lgkmcnt(7)
	v_mfma_f32_16x16x32_f16 a[0:3], v[10:13], a[104:107], a[0:3]
	s_waitcnt lgkmcnt(6)
	v_mfma_f32_16x16x32_f16 a[0:3], v[14:17], a[108:111], a[0:3]
	s_waitcnt lgkmcnt(5)
	v_mfma_f32_16x16x32_f16 a[0:3], v[18:21], a[120:123], a[0:3]
	s_waitcnt lgkmcnt(4)
	v_mfma_f32_16x16x32_f16 a[0:3], v[22:25], a[124:127], a[0:3]
	s_nop 7
	v_accvgpr_read_b32 v0, a0
	v_accvgpr_read_b32 v1, a1
	s_waitcnt vmcnt(0)
	v_add_f32_e32 v0, v180, v0
	v_add_f32_e32 v1, v180, v1
	v_mul_f32_e32 v0, 0x4038aa3b, v0
	v_mul_f32_e32 v1, 0x4038aa3b, v1
	v_exp_f32_e32 v0, v0
	v_exp_f32_e32 v1, v1
	s_waitcnt lgkmcnt(2)
	v_pk_add_f32 v[2:3], v[28:29], 1.0 op_sel_hi:[1,0] neg_lo:[1,0] neg_hi:[1,0]
	s_and_b64 vcc, exec, s[16:17]
	v_add_f32_e32 v0, 1.0, v0
	v_add_f32_e32 v1, 1.0, v1
	v_rcp_f32_e32 v0, v0
	v_rcp_f32_e32 v1, v1
	s_nop 0
	v_pk_fma_f32 v[0:1], v[0:1], 2.0, 1.0 op_sel_hi:[1,0,0] neg_lo:[1,0,0] neg_hi:[1,0,0]
	s_nop 0
	v_pk_mul_f32 v[0:1], v[2:3], v[0:1]
	s_waitcnt lgkmcnt(1)
	v_pk_add_f32 v[2:3], v[30:31], 1.0 op_sel_hi:[1,0] neg_lo:[1,0] neg_hi:[1,0]
	v_pk_fma_f32 v[6:7], v[26:27], v[28:29], v[0:1]
	v_accvgpr_read_b32 v0, a2
	v_accvgpr_read_b32 v1, a3
	v_add_f32_e32 v0, v180, v0
	v_add_f32_e32 v1, v180, v1
	v_mul_f32_e32 v0, 0x4038aa3b, v0
	v_mul_f32_e32 v1, 0x4038aa3b, v1
	v_exp_f32_e32 v0, v0
	v_exp_f32_e32 v1, v1
	v_cvt_pk_f16_f32 v10, v6, v7
	v_add_f32_e32 v0, 1.0, v0
	v_add_f32_e32 v1, 1.0, v1
	v_rcp_f32_e32 v0, v0
	v_rcp_f32_e32 v1, v1
	s_nop 0
	v_pk_fma_f32 v[0:1], v[0:1], 2.0, 1.0 op_sel_hi:[1,0,0] neg_lo:[1,0,0] neg_hi:[1,0,0]
	s_nop 0
	v_pk_mul_f32 v[0:1], v[2:3], v[0:1]
	s_waitcnt lgkmcnt(0)
	v_pk_fma_f32 v[8:9], v[32:33], v[30:31], v[0:1]
	s_nop 0
	v_cvt_pk_f16_f32 v11, v8, v9
	s_cbranch_vccnz .LBB1_172
	global_store_dwordx2 v[178:179], v[10:11], off
	s_add_i32 s70, s40, 4
	s_and_saveexec_b64 s[68:69], s[12:13]
	v_mov_b32_e32 v3, s70
	global_store_dword v[174:175], v3, off
	s_mov_b64 exec, s[68:69]
	s_cbranch_execnz .LBB1_162
.LBB1_161:
	global_store_dwordx2 v[178:179], v[10:11], off sc1
	s_add_i32 s70, s40, 4
	s_and_saveexec_b64 s[68:69], s[12:13]
	v_mov_b32_e32 v3, s70
	global_store_dword v[174:175], v3, off sc1
	s_mov_b64 exec, s[68:69]
.LBB1_162:
	s_add_i32 s40, s40, 4
	v_cvt_f16_f32_e32 v0, v6
	v_cvt_f16_f32_e32 v1, v7
	v_cvt_f16_f32_e32 v2, v8
	v_cvt_f16_f32_e32 v3, v9
	ds_write_b32 v184, v6 offset:25600
	ds_write_b16 v243, v0 offset:128
	ds_write_b32 v250, v7 offset:25600
	v_add_u32_e32 v0, 0x320, v243
	ds_write_b16 v0, v1 offset:128
	ds_write_b32 v185, v8 offset:25600
	v_add_u32_e32 v0, 0x640, v243
	ds_write_b16 v0, v2 offset:128
	ds_write_b32 v251, v9 offset:25600
	v_add_u32_e32 v0, 0x960, v243
	ds_write_b16 v0, v3 offset:128
	s_andn2_b64 vcc, exec, s[18:19]
	s_waitcnt lgkmcnt(0)
	s_barrier
	s_cbranch_vccnz .LBB1_74
	v_and_b32_e32 v1, 64, v246
	v_xor_b32_e32 v0, 1, v246
	v_add_u32_e32 v1, 64, v1
	v_cmp_lt_i32_e32 vcc, v0, v1
	s_nop 1
	v_cndmask_b32_e32 v0, v246, v0, vcc
	v_lshlrev_b32_e32 v12, 2, v0
	v_xor_b32_e32 v0, 2, v246
	v_cmp_lt_i32_e32 vcc, v0, v1
	s_nop 1
	v_cndmask_b32_e32 v0, v246, v0, vcc
	v_lshlrev_b32_e32 v13, 2, v0
	v_xor_b32_e32 v0, 4, v246
	v_cmp_lt_i32_e32 vcc, v0, v1
	s_nop 1
	v_cndmask_b32_e32 v0, v246, v0, vcc
	v_lshlrev_b32_e32 v14, 2, v0
	v_xor_b32_e32 v0, 8, v246
	v_cmp_lt_i32_e32 vcc, v0, v1
	s_nop 1
	v_cndmask_b32_e32 v0, v246, v0, vcc
	v_lshlrev_b32_e32 v15, 2, v0
	v_pk_mul_f32 v[0:1], v[112:113], v[6:7]
	ds_bpermute_b32 v0, v12, v0
	ds_bpermute_b32 v1, v12, v1
	s_waitcnt lgkmcnt(0)
	v_pk_fma_f32 v[0:1], v[112:113], v[6:7], v[0:1]
	ds_bpermute_b32 v2, v13, v0
	ds_bpermute_b32 v3, v13, v1
	s_waitcnt lgkmcnt(0)
	v_pk_add_f32 v[0:1], v[0:1], v[2:3]
	ds_bpermute_b32 v2, v14, v0
	ds_bpermute_b32 v3, v14, v1
	s_waitcnt lgkmcnt(0)
	v_pk_add_f32 v[6:7], v[0:1], v[2:3]
	v_pk_mul_f32 v[0:1], v[112:113], v[8:9]
	ds_bpermute_b32 v0, v12, v0
	ds_bpermute_b32 v1, v12, v1
	ds_bpermute_b32 v10, v15, v6
	ds_bpermute_b32 v11, v15, v7
	s_waitcnt lgkmcnt(2)
	v_pk_fma_f32 v[0:1], v[112:113], v[8:9], v[0:1]
	ds_bpermute_b32 v2, v13, v0
	ds_bpermute_b32 v3, v13, v1
	s_waitcnt lgkmcnt(0)
	v_pk_add_f32 v[0:1], v[0:1], v[2:3]
	ds_bpermute_b32 v2, v14, v0
	ds_bpermute_b32 v3, v14, v1
	s_waitcnt lgkmcnt(0)
	v_pk_add_f32 v[8:9], v[0:1], v[2:3]
	ds_bpermute_b32 v12, v15, v8
	ds_bpermute_b32 v13, v15, v9
	s_and_saveexec_b64 s[16:17], s[14:15]
	s_cbranch_execz .LBB1_169
	v_pk_add_f32 v[0:1], v[6:7], v[10:11]
	s_waitcnt lgkmcnt(0)
	v_pk_add_f32 v[2:3], v[8:9], v[12:13]
	v_accvgpr_read_b32 v6, a240
	ds_write_b128 v6, v[0:3] offset:34560

.Ltg0_redo:
	s_add_i32 s65, s65, 1
	s_cmp_gt_u32 s65, 0xffff
	s_cbranch_scc1 .Ltg0_go
	s_waitcnt lgkmcnt(0)
.Ltg0_poll:
	global_load_dword v250, v[168:169], off sc1
	s_add_i32 s65, s65, 1
	s_cmp_gt_u32 s65, 0xffff
	s_cbranch_scc1 .Ltg0_load
	s_waitcnt vmcnt(0)
	v_cmp_le_u32_e64 s[66:67], s71, v250
	s_cmp_eq_u64 s[66:67], exec
	s_cbranch_scc1 .Ltg0_load
	s_sleep 1
	s_branch .Ltg0_poll
.Ltg0_load:
	buffer_load_dwordx4 v[54:57], v194, s[20:23], 0 offen sc1
	buffer_load_dwordx4 v[50:53], v195, s[20:23], 0 offen sc1
	buffer_load_dwordx4 v[46:49], v196, s[20:23], 0 offen sc1
	buffer_load_dwordx4 v[42:45], v197, s[20:23], 0 offen sc1
	buffer_load_dwordx4 v[38:41], v198, s[20:23], 0 offen sc1
	buffer_load_dwordx4 v[34:37], v199, s[20:23], 0 offen sc1
	buffer_load_dwordx4 v[30:33], v200, s[20:23], 0 offen sc1
	buffer_load_dwordx4 v[26:29], v201, s[20:23], 0 offen sc1
	buffer_load_dwordx4 v[22:25], v202, s[20:23], 0 offen sc1
	buffer_load_dwordx4 v[18:21], v203, s[20:23], 0 offen sc1
	buffer_load_dwordx4 v[14:17], v204, s[20:23], 0 offen sc1
	buffer_load_dwordx4 v[10:13], v205, s[20:23], 0 offen sc1
	buffer_load_dwordx4 v[6:9], v206, s[20:23], 0 offen sc1
	s_waitcnt vmcnt(0) lgkmcnt(0)
	s_branch .Ltg0_entry

.Ltg1_poll:
	global_load_dword v255, v[168:169], off sc1
	s_add_i32 s65, s65, 1
	s_cmp_gt_u32 s65, 0xffff
	s_cbranch_scc1 .Ltg1_load
	s_waitcnt vmcnt(0)
	v_cmp_le_u32_e64 s[66:67], s71, v255
	s_cmp_eq_u64 s[66:67], exec
	s_cbranch_scc1 .Ltg1_load
	s_sleep 1
	s_branch .Ltg1_poll
.Ltg1_load:
	buffer_load_dwordx4 v[0:3], v229, s[20:23], 0 offen sc1
	buffer_load_dwordx4 v[6:9], v230, s[20:23], 0 offen sc1
	buffer_load_dwordx4 v[10:13], v231, s[20:23], 0 offen sc1
	buffer_load_dwordx4 v[14:17], v232, s[20:23], 0 offen sc1
	buffer_load_dwordx4 v[18:21], v233, s[20:23], 0 offen sc1
	buffer_load_dwordx4 v[22:25], v234, s[20:23], 0 offen sc1
	buffer_load_dwordx4 v[26:29], v235, s[20:23], 0 offen sc1
	buffer_load_dwordx4 v[30:33], v236, s[20:23], 0 offen sc1
	buffer_load_dwordx4 v[34:37], v237, s[20:23], 0 offen sc1
	buffer_load_dwordx4 v[38:41], v238, s[20:23], 0 offen sc1
	buffer_load_dwordx4 v[42:45], v239, s[20:23], 0 offen sc1
	buffer_load_dwordx4 v[46:49], v240, s[20:23], 0 offen sc1
	buffer_load_dwordx4 v[50:53], v241, s[20:23], 0 offen sc1
	s_waitcnt vmcnt(0) lgkmcnt(0)
	s_branch .Ltg1_entry

.Ltg2_load:
	buffer_load_dwordx4 v[0:3], v194, s[20:23], 0 offen sc1
	buffer_load_dwordx4 v[6:9], v195, s[20:23], 0 offen sc1
	buffer_load_dwordx4 v[10:13], v196, s[20:23], 0 offen sc1
	buffer_load_dwordx4 v[14:17], v197, s[20:23], 0 offen sc1
	buffer_load_dwordx4 v[18:21], v198, s[20:23], 0 offen sc1
	buffer_load_dwordx4 v[22:25], v199, s[20:23], 0 offen sc1
	buffer_load_dwordx4 v[26:29], v200, s[20:23], 0 offen sc1
	buffer_load_dwordx4 v[30:33], v201, s[20:23], 0 offen sc1
	buffer_load_dwordx4 v[34:37], v202, s[20:23], 0 offen sc1
	buffer_load_dwordx4 v[38:41], v203, s[20:23], 0 offen sc1
	buffer_load_dwordx4 v[42:45], v204, s[20:23], 0 offen sc1
	buffer_load_dwordx4 v[46:49], v205, s[20:23], 0 offen sc1
	buffer_load_dwordx4 v[50:53], v206, s[20:23], 0 offen sc1
	ds_read_b128 v[54:57], v208 offset:34832
	ds_read_b128 v[64:67], v208 offset:48144
	ds_read_b128 v[68:71], v209 offset:34832
	ds_read_b128 v[72:75], v209 offset:48144
	ds_read_b128 v[78:81], v210 offset:34832
	ds_read_b128 v[82:85], v210 offset:48144
	ds_read_b128 v[86:89], v211 offset:34832
	ds_read_b128 v[90:93], v211 offset:48144
	ds_read_b128 v[94:97], v212 offset:34832
	ds_read_b128 v[98:101], v212 offset:48144
	ds_read_b128 v[102:105], v213 offset:34832
	ds_read_b128 v[106:109], v213 offset:48144
	ds_read_b128 v[114:117], v214 offset:34832
	ds_read_b128 v[118:121], v214 offset:48144
	ds_read_b128 v[122:125], v215 offset:34832
	ds_read_b128 v[126:129], v215 offset:48144
	ds_read_b128 v[130:133], v216 offset:34832
	ds_read_b128 v[134:137], v216 offset:48144
	ds_read_b128 v[138:141], v217 offset:34832
	ds_read_b128 v[142:145], v217 offset:48144
	ds_read_b128 v[146:149], v218 offset:34832
	ds_read_b128 v[150:153], v218 offset:48144
	ds_read_b128 v[154:157], v219 offset:34832
	ds_read_b128 v[158:161], v219 offset:48144
	ds_read_b128 v[162:165], v220 offset:34832
	ds_read_b128 v[190:193], v220 offset:48144
	s_waitcnt vmcnt(0) lgkmcnt(0)
	s_branch .Ltg2_entry
